# speedup vs baseline: 1.0251x; 1.0070x over previous
.LBB9_4:
	s_load_dwordx4 s[32:35], s[0:1], 0x18
	s_load_dword s36, s[0:1], 0x28
	s_load_dwordx4 s[4:7], s[0:1], 0x60
	s_load_dwordx2 s[12:13], s[0:1], 0x10
	s_ashr_i32 s2, s2, 3
	s_add_i32 s2, s3, s2
	s_abs_i32 s3, s2
	s_waitcnt lgkmcnt(0)
	s_lshl_b32 s26, s7, 7
	s_lshl_b32 s24, s26, 5
	s_mov_b32 s27, 0
	s_cmp_eq_u32 s12, 0x800
	s_cselect_b32 s25, s24, 32
	s_cselect_b32 s26, s26, 1
	s_cselect_b32 s12, 32, s12
	s_mov_b32 s92, s6
	s_mov_b32 s93, s7
	v_cvt_f32_u32_e32 v100, s6
	v_cvt_f32_u32_e32 v101, s7
	v_cvt_f32_u32_e32 v102, s2
	v_rcp_iflag_f32_e32 v100, v100
	v_rcp_iflag_f32_e32 v101, v101
	v_add_f32_e32 v102, 0.5, v102
	s_nop 0
	v_mul_f32_e32 v102, v102, v100
	v_cvt_u32_f32_e32 v102, v102
	v_cvt_f32_u32_e32 v100, v102
	v_add_f32_e32 v100, 0.5, v100
	v_readfirstlane_b32 s94, v102
	v_mul_f32_e32 v100, v100, v101
	v_cvt_u32_f32_e32 v100, v100
	s_mul_i32 s90, s94, s92
	s_sub_i32 s90, s2, s90
	v_readfirstlane_b32 s95, v100
	s_nop 0
	s_mul_i32 s91, s95, s93
	s_sub_i32 s91, s94, s91
	s_mov_b32 s3, s94
	s_mov_b32 s14, s90
	s_mov_b32 s16, s95
	s_mov_b32 s2, s91
	v_lshlrev_b32_e32 v3, 3, v0
	v_lshrrev_b32_e32 v2, 2, v0
	v_and_b32_e32 v8, 24, v3
	v_mov_b32_e32 v9, 0
	v_lshlrev_b32_e32 v3, 1, v8
	v_lshrrev_b32_e32 v23, 6, v0
	v_and_b32_e32 v22, 31, v0
	s_lshl_b32 s15, s2, 7
	s_mul_i32 s2, s16, s4
	s_mul_i32 s26, s2, s26
	s_ashr_i32 s3, s2, 31
	v_or_b32_e32 v1, s15, v2
	s_ashr_i32 s17, s15, 31
	v_lshl_add_u64 v[4:5], s[26:27], 0, v[8:9]
	s_mul_i32 s20, s12, s17
	v_mad_u64_u32 v[4:5], s[18:19], s12, v1, v[4:5]
	v_mul_lo_u32 v1, s13, v1
	s_lshl_b64 s[6:7], s[12:13], 6
	v_add3_u32 v5, v1, v5, s20
	v_lshl_add_u64 v[6:7], v[4:5], 0, s[6:7]
	v_lshlrev_b64 v[4:5], 1, v[4:5]
	v_lshl_add_u64 v[12:13], s[10:11], 0, v[4:5]
	v_lshl_add_u64 v[14:15], s[8:9], 0, v[4:5]
	s_lshl_b64 s[6:7], s[12:13], 7
	v_lshl_add_u64 v[10:11], v[6:7], 1, s[8:9]
	v_lshl_add_u64 v[16:17], v[12:13], 0, s[6:7]
	global_load_dwordx4 v[124:127], v[14:15], off
	global_load_dwordx4 v[128:131], v[12:13], off
	global_load_dwordx4 v[132:135], v[10:11], off
	global_load_dwordx4 v[136:139], v[16:17], off
	s_load_dwordx2 s[6:7], s[0:1], 0x38
	s_movk_i32 s9, 0x50
	v_and_b32_e32 v1, 63, v0
	s_nop 7
	v_bfe_u32 v24, v0, 5, 1
	v_mad_u32_u24 v112, v2, s9, v3
	s_mov_b32 s10, s36
	s_lshr_b32 s3, s3, 28
	s_ashr_i32 s8, s4, 31
	s_add_i32 s2, s2, s3
	s_lshr_b32 s8, s8, 27
	s_waitcnt lgkmcnt(0)
	s_ashr_i32 s12, s10, 31
	s_lshr_b32 s12, s12, 28
	s_ashr_i32 s2, s2, 4
	s_add_i32 s4, s4, s8
	s_add_i32 s10, s10, s12
	s_ashr_i32 s3, s2, 31
	s_ashr_i32 s4, s4, 5
	v_lshl_or_b32 v6, s14, 2, v23
	s_ashr_i32 s10, s10, 4
	v_mov_b32_e32 v4, s2
	v_mov_b32_e32 v5, s3
	s_add_i32 s8, s4, -1
	v_mad_i64_i32 v[4:5], s[2:3], v6, s10, v[4:5]
	s_min_i32 s11, s8, 2
	v_lshlrev_b64 v[4:5], 10, v[4:5]
	v_lshl_or_b32 v4, v1, 4, v4
	s_mul_i32 s2, s11, s25
	v_lshl_add_u64 v[18:19], s[32:33], 0, v[4:5]
	s_ashr_i32 s3, s2, 31
	s_lshl_b32 s28, s25, 1
	s_mov_b32 s29, 0
	v_lshl_add_u64 v[116:117], v[14:15], 0, s[28:29]
	v_lshl_add_u64 v[118:119], v[12:13], 0, s[28:29]
	v_lshl_add_u64 v[120:121], v[10:11], 0, s[28:29]
	v_lshl_add_u64 v[122:123], v[16:17], 0, s[28:29]
	global_load_dwordx4 v[44:47], v[116:117], off
	global_load_dwordx4 v[48:51], v[118:119], off
	global_load_dwordx4 v[32:35], v[120:121], off
	global_load_dwordx4 v[28:31], v[122:123], off
	v_lshl_add_u64 v[20:21], s[34:35], 0, v[4:5]
	global_load_dwordx4 v[64:67], v[18:19], off
	global_load_dwordx4 v[36:39], v[18:19], off offset:1024
	global_load_dwordx4 v[80:83], v[20:21], off
	global_load_dwordx4 v[40:43], v[20:21], off offset:1024
	global_load_dwordx4 v[68:71], v[18:19], off offset:2048
	global_load_dwordx4 v[76:79], v[20:21], off offset:2048
	s_lshl_b64 s[2:3], s[2:3], 1
	v_lshl_add_u64 v[26:27], v[14:15], 0, s[2:3]
	v_lshl_add_u64 v[4:5], v[10:11], 0, s[2:3]
	v_lshl_add_u64 v[6:7], v[12:13], 0, s[2:3]
	v_lshl_add_u64 v[8:9], v[16:17], 0, s[2:3]
	global_load_dwordx4 v[60:63], v[26:27], off
	global_load_dwordx4 v[56:59], v[4:5], off
	global_load_dwordx4 v[72:75], v[6:7], off
	global_load_dwordx4 v[52:55], v[8:9], off
	v_accvgpr_write_b32 a48, 0
	v_accvgpr_write_b32 a49, 0
	v_accvgpr_write_b32 a50, 0
	v_accvgpr_write_b32 a51, 0
	v_accvgpr_write_b32 a52, 0
	v_accvgpr_write_b32 a53, 0
	v_accvgpr_write_b32 a54, 0
	v_accvgpr_write_b32 a55, 0
	v_accvgpr_write_b32 a56, 0
	v_accvgpr_write_b32 a57, 0
	v_accvgpr_write_b32 a58, 0
	v_accvgpr_write_b32 a59, 0
	v_accvgpr_write_b32 a60, 0
	v_accvgpr_write_b32 a61, 0
	v_accvgpr_write_b32 a62, 0
	v_accvgpr_write_b32 a63, 0
	v_accvgpr_write_b32 a32, 0
	v_accvgpr_write_b32 a33, 0
	v_accvgpr_write_b32 a34, 0
	v_accvgpr_write_b32 a35, 0
	v_accvgpr_write_b32 a36, 0
	v_accvgpr_write_b32 a37, 0
	v_accvgpr_write_b32 a38, 0
	v_accvgpr_write_b32 a39, 0
	v_accvgpr_write_b32 a40, 0
	v_accvgpr_write_b32 a41, 0
	v_accvgpr_write_b32 a42, 0
	v_accvgpr_write_b32 a43, 0
	v_accvgpr_write_b32 a44, 0
	v_accvgpr_write_b32 a45, 0
	v_accvgpr_write_b32 a46, 0
	v_accvgpr_write_b32 a47, 0
	v_accvgpr_write_b32 a16, 0
	v_accvgpr_write_b32 a17, 0
	v_accvgpr_write_b32 a18, 0
	v_accvgpr_write_b32 a19, 0
	v_accvgpr_write_b32 a20, 0
	v_accvgpr_write_b32 a21, 0
	v_accvgpr_write_b32 a22, 0
	v_accvgpr_write_b32 a23, 0
	v_accvgpr_write_b32 a24, 0
	v_accvgpr_write_b32 a25, 0
	v_accvgpr_write_b32 a26, 0
	v_accvgpr_write_b32 a27, 0
	v_accvgpr_write_b32 a28, 0
	v_accvgpr_write_b32 a29, 0
	v_accvgpr_write_b32 a30, 0
	v_accvgpr_write_b32 a31, 0
	v_accvgpr_write_b32 a0, 0
	v_accvgpr_write_b32 a1, 0
	v_accvgpr_write_b32 a2, 0
	v_accvgpr_write_b32 a3, 0
	v_accvgpr_write_b32 a4, 0
	v_accvgpr_write_b32 a5, 0
	v_accvgpr_write_b32 a6, 0
	v_accvgpr_write_b32 a7, 0
	v_accvgpr_write_b32 a8, 0
	v_accvgpr_write_b32 a9, 0
	v_accvgpr_write_b32 a10, 0
	v_accvgpr_write_b32 a11, 0
	v_accvgpr_write_b32 a12, 0
	v_accvgpr_write_b32 a13, 0
	v_accvgpr_write_b32 a14, 0
	v_accvgpr_write_b32 a15, 0
	s_waitcnt vmcnt(17)
	ds_write_b128 v112, v[124:127]
	s_waitcnt vmcnt(16)
	ds_write_b128 v112, v[128:131] offset:10240
	s_waitcnt vmcnt(15)
	ds_write_b128 v112, v[132:135] offset:5120
	s_waitcnt vmcnt(14)
	ds_write_b128 v112, v[136:139] offset:15360
	s_waitcnt lgkmcnt(0)
	s_barrier
	v_lshlrev_b32_e32 v4, 4, v24
	v_mad_u32_u24 v6, v22, s9, v4
	ds_read_b128 v[84:87], v6 offset:7680
	ds_read_b128 v[92:95], v6 offset:5120
	ds_read_b128 v[88:91], v6 offset:17920
	ds_read_b128 v[96:99], v6 offset:15360
	ds_read_b128 v[100:103], v6 offset:2560
	ds_read_b128 v[104:107], v6
	ds_read_b128 v[108:111], v6 offset:12800
	ds_read_b128 v[112:115], v6 offset:10240
	v_mul_u32_u24_e32 v2, 0x50, v2
	v_mul_u32_u24_e32 v5, 0x50, v22
	s_mov_b32 s2, 4
	s_nop 7
	v_add_u32_e32 v25, v4, v5
	v_add_u32_e32 v26, v3, v2
	s_add_i32 s3, s4, -2
	s_cmp_gt_i32 s2, s3
	s_cbranch_scc1 .Ltail_LBB9
.LBB9_6:
	s_waitcnt vmcnt(9) lgkmcnt(0)
	v_mfma_f32_32x32x16_f16 a[0:15], v[112:115], v[64:67], a[0:15]
	s_add_i32 s3, s2, -3
	s_min_i32 s3, s3, s8
	s_lshl_b32 s3, s3, 1
	ds_read_b128 v[116:119], v25 offset:10272
	s_or_b32 s10, s3, 1
	s_ashr_i32 s11, s10, 31
	s_lshl_b64 s[10:11], s[10:11], 10
	v_lshl_add_u64 v[2:3], v[18:19], 0, s[10:11]
	v_lshl_add_u64 v[6:7], v[20:21], 0, s[10:11]
	s_waitcnt vmcnt(7)
	v_mfma_f32_32x32x16_f16 a[0:15], v[104:107], v[80:83], a[0:15]
	ds_read_b128 v[112:115], v25 offset:32
	v_mfma_f32_32x32x16_f16 a[0:15], v[104:107], v[64:67], a[0:15]
	ds_read_b128 v[120:123], v25 offset:12832
	ds_write_b128 v26, v[44:47] offset:20480
	v_mfma_f32_32x32x16_f16 a[16:31], v[108:111], v[64:67], a[16:31]
	ds_read_b128 v[104:107], v25 offset:2592
	v_mfma_f32_32x32x16_f16 a[16:31], v[100:103], v[80:83], a[16:31]
	ds_read_b128 v[108:111], v25 offset:15392
	ds_write_b128 v26, v[48:51] offset:30720
	v_mfma_f32_32x32x16_f16 a[16:31], v[100:103], v[64:67], a[16:31]
	ds_read_b128 v[124:127], v25 offset:5152
	v_mfma_f32_32x32x16_f16 a[32:47], v[96:99], v[64:67], a[32:47]
	ds_read_b128 v[100:103], v25 offset:17952
	ds_write_b128 v26, v[32:35] offset:25600
	v_mfma_f32_32x32x16_f16 a[32:47], v[92:95], v[80:83], a[32:47]
	ds_read_b128 v[96:99], v25 offset:7712
	v_mfma_f32_32x32x16_f16 a[32:47], v[92:95], v[64:67], a[32:47]
	ds_write_b128 v26, v[28:31] offset:35840
	global_load_dwordx4 v[2:5], v[2:3], off
	s_nop 0
	global_load_dwordx4 v[6:9], v[6:7], off
	v_mfma_f32_32x32x16_f16 a[48:63], v[88:91], v[64:67], a[48:63]
	v_mfma_f32_32x32x16_f16 a[48:63], v[84:87], v[80:83], a[48:63]
	v_mfma_f32_32x32x16_f16 a[48:63], v[84:87], v[64:67], a[48:63]
	s_add_i32 s3, s2, -1
	s_min_i32 s9, s3, s8
	s_mul_i32 s10, s9, s25
	s_ashr_i32 s11, s10, 31
	s_lshl_b64 s[10:11], s[10:11], 1
	v_lshl_add_u64 v[28:29], v[14:15], 0, s[10:11]
	s_waitcnt lgkmcnt(0)
	s_barrier
	global_load_dwordx4 v[44:47], v[28:29], off
	v_mfma_f32_32x32x16_f16 a[0:15], v[116:119], v[36:39], a[0:15]
	s_add_i32 s3, s2, -2
	v_lshl_add_u64 v[28:29], v[10:11], 0, s[10:11]
	v_lshl_add_u64 v[30:31], v[12:13], 0, s[10:11]
	v_lshl_add_u64 v[64:65], v[16:17], 0, s[10:11]
	s_min_i32 s10, s3, s8
	ds_read_b128 v[84:87], v25 offset:30720
	s_lshl_b32 s10, s10, 1
	s_ashr_i32 s11, s10, 31
	s_lshl_b64 s[12:13], s[10:11], 10
	v_lshl_add_u64 v[66:67], v[18:19], 0, s[12:13]
	v_lshl_add_u64 v[80:81], v[20:21], 0, s[12:13]
	global_load_dwordx4 v[48:51], v[30:31], off
	s_waitcnt vmcnt(10)
	v_mfma_f32_32x32x16_f16 a[0:15], v[112:115], v[40:43], a[0:15]
	ds_read_b128 v[88:91], v25 offset:20480
	global_load_dwordx4 v[32:35], v[28:29], off
	v_mfma_f32_32x32x16_f16 a[0:15], v[112:115], v[36:39], a[0:15]
	ds_read_b128 v[92:95], v25 offset:33280
	global_load_dwordx4 v[28:31], v[64:65], off
	v_mfma_f32_32x32x16_f16 a[16:31], v[120:123], v[36:39], a[16:31]
	ds_read_b128 v[112:115], v25 offset:23040
	v_mfma_f32_32x32x16_f16 a[16:31], v[104:107], v[40:43], a[16:31]
	ds_read_b128 v[116:119], v25 offset:35840
	v_mfma_f32_32x32x16_f16 a[16:31], v[104:107], v[36:39], a[16:31]
	ds_read_b128 v[120:123], v25 offset:25600
	v_mfma_f32_32x32x16_f16 a[32:47], v[108:111], v[36:39], a[32:47]
	ds_read_b128 v[104:107], v25 offset:38400
	v_mfma_f32_32x32x16_f16 a[32:47], v[124:127], v[40:43], a[32:47]
	ds_read_b128 v[108:111], v25 offset:28160
	v_mfma_f32_32x32x16_f16 a[32:47], v[124:127], v[36:39], a[32:47]
	global_load_dwordx4 v[64:67], v[66:67], off
	s_nop 0
	global_load_dwordx4 v[80:83], v[80:81], off
	v_mfma_f32_32x32x16_f16 a[48:63], v[100:103], v[36:39], a[48:63]
	v_mfma_f32_32x32x16_f16 a[48:63], v[96:99], v[40:43], a[48:63]
	v_mfma_f32_32x32x16_f16 a[48:63], v[96:99], v[36:39], a[48:63]
	s_waitcnt vmcnt(9) lgkmcnt(7)
	v_mfma_f32_32x32x16_f16 a[0:15], v[84:87], v[68:71], a[0:15]
	ds_read_b128 v[96:99], v25 offset:30752
	s_or_b32 s10, s10, 1
	s_ashr_i32 s11, s10, 31
	s_lshl_b64 s[10:11], s[10:11], 10
	v_lshl_add_u64 v[36:37], v[18:19], 0, s[10:11]
	v_lshl_add_u64 v[40:41], v[20:21], 0, s[10:11]
	s_waitcnt vmcnt(8) lgkmcnt(7)
	v_mfma_f32_32x32x16_f16 a[0:15], v[88:91], v[76:79], a[0:15]
	ds_read_b128 v[84:87], v25 offset:20512
	v_mfma_f32_32x32x16_f16 a[0:15], v[88:91], v[68:71], a[0:15]
	ds_read_b128 v[124:127], v25 offset:33312
	s_waitcnt vmcnt(11)
	ds_write_b128 v26, v[60:63]
	s_waitcnt lgkmcnt(9)
	v_mfma_f32_32x32x16_f16 a[16:31], v[92:95], v[68:71], a[16:31]
	ds_read_b128 v[88:91], v25 offset:23072
	s_waitcnt lgkmcnt(9)
	v_mfma_f32_32x32x16_f16 a[16:31], v[112:115], v[76:79], a[16:31]
	ds_read_b128 v[128:131], v25 offset:35872
	s_waitcnt vmcnt(9)
	ds_write_b128 v26, v[72:75] offset:10240
	v_mfma_f32_32x32x16_f16 a[16:31], v[112:115], v[68:71], a[16:31]
	ds_read_b128 v[132:135], v25 offset:25632
	s_waitcnt lgkmcnt(11)
	v_mfma_f32_32x32x16_f16 a[32:47], v[116:119], v[68:71], a[32:47]
	ds_read_b128 v[136:139], v25 offset:38432
	ds_write_b128 v26, v[56:59] offset:5120
	s_waitcnt lgkmcnt(12)
	v_mfma_f32_32x32x16_f16 a[32:47], v[120:123], v[76:79], a[32:47]
	ds_read_b128 v[116:119], v25 offset:28192
	v_mfma_f32_32x32x16_f16 a[32:47], v[120:123], v[68:71], a[32:47]
	s_waitcnt vmcnt(10)
	ds_write_b128 v26, v[52:55] offset:15360
	global_load_dwordx4 v[36:39], v[36:37], off
	s_nop 0
	global_load_dwordx4 v[40:43], v[40:41], off
	s_waitcnt lgkmcnt(13)
	v_mfma_f32_32x32x16_f16 a[48:63], v[104:107], v[68:71], a[48:63]
	s_waitcnt lgkmcnt(12)
	v_mfma_f32_32x32x16_f16 a[48:63], v[108:111], v[76:79], a[48:63]
	v_mfma_f32_32x32x16_f16 a[48:63], v[108:111], v[68:71], a[48:63]
	s_min_i32 s10, s2, s8
	s_mul_i32 s10, s10, s25
	s_ashr_i32 s11, s10, 31
	s_lshl_b64 s[10:11], s[10:11], 1
	v_lshl_add_u64 v[52:53], v[14:15], 0, s[10:11]
	s_waitcnt lgkmcnt(0)
	s_barrier
	global_load_dwordx4 v[60:63], v[52:53], off
	s_waitcnt vmcnt(10)
	v_mfma_f32_32x32x16_f16 a[0:15], v[96:99], v[2:5], a[0:15]
	ds_read_b128 v[112:115], v25 offset:10240
	v_lshl_add_u64 v[52:53], v[10:11], 0, s[10:11]
	v_lshl_add_u64 v[54:55], v[12:13], 0, s[10:11]
	v_lshl_add_u64 v[68:69], v[16:17], 0, s[10:11]
	s_lshl_b32 s10, s9, 1
	s_ashr_i32 s11, s10, 31
	s_lshl_b64 s[10:11], s[10:11], 10
	v_lshl_add_u64 v[70:71], v[18:19], 0, s[10:11]
	v_lshl_add_u64 v[76:77], v[20:21], 0, s[10:11]
	global_load_dwordx4 v[72:75], v[54:55], off
	s_waitcnt vmcnt(10)
	v_mfma_f32_32x32x16_f16 a[0:15], v[84:87], v[6:9], a[0:15]
	ds_read_b128 v[104:107], v25
	global_load_dwordx4 v[56:59], v[52:53], off
	v_mfma_f32_32x32x16_f16 a[0:15], v[84:87], v[2:5], a[0:15]
	ds_read_b128 v[108:111], v25 offset:12800
	global_load_dwordx4 v[52:55], v[68:69], off
	v_mfma_f32_32x32x16_f16 a[16:31], v[124:127], v[2:5], a[16:31]
	ds_read_b128 v[100:103], v25 offset:2560
	v_mfma_f32_32x32x16_f16 a[16:31], v[88:91], v[6:9], a[16:31]
	ds_read_b128 v[96:99], v25 offset:15360
	v_mfma_f32_32x32x16_f16 a[16:31], v[88:91], v[2:5], a[16:31]
	ds_read_b128 v[92:95], v25 offset:5120
	v_mfma_f32_32x32x16_f16 a[32:47], v[128:131], v[2:5], a[32:47]
	ds_read_b128 v[88:91], v25 offset:17920
	v_mfma_f32_32x32x16_f16 a[32:47], v[132:135], v[6:9], a[32:47]
	ds_read_b128 v[84:87], v25 offset:7680
	v_mfma_f32_32x32x16_f16 a[32:47], v[132:135], v[2:5], a[32:47]
	global_load_dwordx4 v[68:71], v[70:71], off
	s_nop 0
	global_load_dwordx4 v[76:79], v[76:77], off
	v_mfma_f32_32x32x16_f16 a[48:63], v[136:139], v[2:5], a[48:63]
	v_mfma_f32_32x32x16_f16 a[48:63], v[116:119], v[6:9], a[48:63]
	v_mfma_f32_32x32x16_f16 a[48:63], v[116:119], v[2:5], a[48:63]
	s_add_i32 s2, s2, 2
	s_add_i32 s3, s4, -2
	s_cmp_le_i32 s2, s3
	s_cbranch_scc1 .LBB9_6
.Ltail_LBB9:
	s_waitcnt lgkmcnt(0)
	s_waitcnt vmcnt(9)
	v_mfma_f32_32x32x16_f16 a[0:15], v[112:115], v[64:67], a[0:15]
	s_add_i32 s3, s2, -3
	s_min_i32 s3, s3, s8
	s_lshl_b32 s3, s3, 1
	ds_read_b128 v[116:119], v25 offset:10272
	s_or_b32 s10, s3, 1
	s_ashr_i32 s11, s10, 31
	s_lshl_b64 s[10:11], s[10:11], 10
	v_lshl_add_u64 v[2:3], v[18:19], 0, s[10:11]
	v_lshl_add_u64 v[6:7], v[20:21], 0, s[10:11]
	s_waitcnt vmcnt(7)
	v_mfma_f32_32x32x16_f16 a[0:15], v[104:107], v[80:83], a[0:15]
	ds_read_b128 v[112:115], v25 offset:32
	v_mfma_f32_32x32x16_f16 a[0:15], v[104:107], v[64:67], a[0:15]
	ds_read_b128 v[120:123], v25 offset:12832
	ds_write_b128 v26, v[44:47] offset:20480
	v_mfma_f32_32x32x16_f16 a[16:31], v[108:111], v[64:67], a[16:31]
	ds_read_b128 v[104:107], v25 offset:2592
	v_mfma_f32_32x32x16_f16 a[16:31], v[100:103], v[80:83], a[16:31]
	ds_read_b128 v[108:111], v25 offset:15392
	ds_write_b128 v26, v[48:51] offset:30720
	v_mfma_f32_32x32x16_f16 a[16:31], v[100:103], v[64:67], a[16:31]
	ds_read_b128 v[124:127], v25 offset:5152
	v_mfma_f32_32x32x16_f16 a[32:47], v[96:99], v[64:67], a[32:47]
	ds_read_b128 v[100:103], v25 offset:17952
	ds_write_b128 v26, v[32:35] offset:25600
	v_mfma_f32_32x32x16_f16 a[32:47], v[92:95], v[80:83], a[32:47]
	ds_read_b128 v[96:99], v25 offset:7712
	v_mfma_f32_32x32x16_f16 a[32:47], v[92:95], v[64:67], a[32:47]
	ds_write_b128 v26, v[28:31] offset:35840
	global_load_dwordx4 v[2:5], v[2:3], off
	s_nop 0
	global_load_dwordx4 v[6:9], v[6:7], off
	v_mfma_f32_32x32x16_f16 a[48:63], v[88:91], v[64:67], a[48:63]
	v_mfma_f32_32x32x16_f16 a[48:63], v[84:87], v[80:83], a[48:63]
	v_mfma_f32_32x32x16_f16 a[48:63], v[84:87], v[64:67], a[48:63]
	s_add_i32 s3, s2, -1
	s_min_i32 s9, s3, s8
	s_mul_i32 s10, s9, s25
	s_ashr_i32 s11, s10, 31
	s_lshl_b64 s[10:11], s[10:11], 1
	v_lshl_add_u64 v[28:29], v[14:15], 0, s[10:11]
	s_waitcnt lgkmcnt(0)
	s_barrier
	global_load_dwordx4 v[44:47], v[28:29], off
	v_mfma_f32_32x32x16_f16 a[0:15], v[116:119], v[36:39], a[0:15]
	s_add_i32 s3, s2, -2
	v_lshl_add_u64 v[28:29], v[10:11], 0, s[10:11]
	v_lshl_add_u64 v[30:31], v[12:13], 0, s[10:11]
	v_lshl_add_u64 v[64:65], v[16:17], 0, s[10:11]
	s_min_i32 s10, s3, s8
	ds_read_b128 v[84:87], v25 offset:30720
	s_lshl_b32 s10, s10, 1
	s_ashr_i32 s11, s10, 31
	s_lshl_b64 s[12:13], s[10:11], 10
	v_lshl_add_u64 v[66:67], v[18:19], 0, s[12:13]
	v_lshl_add_u64 v[80:81], v[20:21], 0, s[12:13]
	global_load_dwordx4 v[48:51], v[30:31], off
	s_waitcnt vmcnt(10)
	v_mfma_f32_32x32x16_f16 a[0:15], v[112:115], v[40:43], a[0:15]
	ds_read_b128 v[88:91], v25 offset:20480
	global_load_dwordx4 v[32:35], v[28:29], off
	v_mfma_f32_32x32x16_f16 a[0:15], v[112:115], v[36:39], a[0:15]
	ds_read_b128 v[92:95], v25 offset:33280
	global_load_dwordx4 v[28:31], v[64:65], off
	v_mfma_f32_32x32x16_f16 a[16:31], v[120:123], v[36:39], a[16:31]
	ds_read_b128 v[112:115], v25 offset:23040
	v_mfma_f32_32x32x16_f16 a[16:31], v[104:107], v[40:43], a[16:31]
	ds_read_b128 v[116:119], v25 offset:35840
	v_mfma_f32_32x32x16_f16 a[16:31], v[104:107], v[36:39], a[16:31]
	ds_read_b128 v[120:123], v25 offset:25600
	v_mfma_f32_32x32x16_f16 a[32:47], v[108:111], v[36:39], a[32:47]
	ds_read_b128 v[104:107], v25 offset:38400
	v_mfma_f32_32x32x16_f16 a[32:47], v[124:127], v[40:43], a[32:47]
	ds_read_b128 v[108:111], v25 offset:28160
	v_mfma_f32_32x32x16_f16 a[32:47], v[124:127], v[36:39], a[32:47]
	global_load_dwordx4 v[64:67], v[66:67], off
	s_nop 0
	global_load_dwordx4 v[80:83], v[80:81], off
	v_mfma_f32_32x32x16_f16 a[48:63], v[100:103], v[36:39], a[48:63]
	v_mfma_f32_32x32x16_f16 a[48:63], v[96:99], v[40:43], a[48:63]
	v_mfma_f32_32x32x16_f16 a[48:63], v[96:99], v[36:39], a[48:63]
	s_waitcnt lgkmcnt(7)
	s_waitcnt vmcnt(9)
	v_mfma_f32_32x32x16_f16 a[0:15], v[84:87], v[68:71], a[0:15]
	ds_read_b128 v[96:99], v25 offset:30752
	s_or_b32 s10, s10, 1
	s_ashr_i32 s11, s10, 31
	s_lshl_b64 s[10:11], s[10:11], 10
	v_lshl_add_u64 v[36:37], v[18:19], 0, s[10:11]
	v_lshl_add_u64 v[40:41], v[20:21], 0, s[10:11]
	s_waitcnt lgkmcnt(7)
	s_waitcnt vmcnt(8)
	v_mfma_f32_32x32x16_f16 a[0:15], v[88:91], v[76:79], a[0:15]
	ds_read_b128 v[84:87], v25 offset:20512
	v_mfma_f32_32x32x16_f16 a[0:15], v[88:91], v[68:71], a[0:15]
	ds_read_b128 v[124:127], v25 offset:33312
	s_waitcnt vmcnt(11)
	ds_write_b128 v26, v[60:63]
	s_waitcnt lgkmcnt(9)
	v_mfma_f32_32x32x16_f16 a[16:31], v[92:95], v[68:71], a[16:31]
	ds_read_b128 v[88:91], v25 offset:23072
	s_waitcnt lgkmcnt(9)
	v_mfma_f32_32x32x16_f16 a[16:31], v[112:115], v[76:79], a[16:31]
	ds_read_b128 v[128:131], v25 offset:35872
	s_waitcnt vmcnt(9)
	ds_write_b128 v26, v[72:75] offset:10240
	v_mfma_f32_32x32x16_f16 a[16:31], v[112:115], v[68:71], a[16:31]
	ds_read_b128 v[132:135], v25 offset:25632
	s_waitcnt lgkmcnt(11)
	v_mfma_f32_32x32x16_f16 a[32:47], v[116:119], v[68:71], a[32:47]
	ds_read_b128 v[136:139], v25 offset:38432
	ds_write_b128 v26, v[56:59] offset:5120
	s_waitcnt lgkmcnt(12)
	v_mfma_f32_32x32x16_f16 a[32:47], v[120:123], v[76:79], a[32:47]
	ds_read_b128 v[116:119], v25 offset:28192
	v_mfma_f32_32x32x16_f16 a[32:47], v[120:123], v[68:71], a[32:47]
	s_waitcnt vmcnt(8)
	ds_write_b128 v26, v[52:55] offset:15360
	global_load_dwordx4 v[36:39], v[36:37], off
	s_nop 0
	global_load_dwordx4 v[40:43], v[40:41], off
	s_waitcnt lgkmcnt(13)
	v_mfma_f32_32x32x16_f16 a[48:63], v[104:107], v[68:71], a[48:63]
	s_waitcnt lgkmcnt(12)
	v_mfma_f32_32x32x16_f16 a[48:63], v[108:111], v[76:79], a[48:63]
	v_mfma_f32_32x32x16_f16 a[48:63], v[108:111], v[68:71], a[48:63]
	s_min_i32 s10, s2, s8
	s_mul_i32 s10, s10, s25
	s_ashr_i32 s11, s10, 31
	s_lshl_b64 s[10:11], s[10:11], 1
	v_lshl_add_u64 v[52:53], v[14:15], 0, s[10:11]
	s_waitcnt lgkmcnt(0)
	s_barrier
	s_waitcnt vmcnt(9)
	v_mfma_f32_32x32x16_f16 a[0:15], v[96:99], v[2:5], a[0:15]
	ds_read_b128 v[112:115], v25 offset:10240
	v_lshl_add_u64 v[52:53], v[10:11], 0, s[10:11]
	v_lshl_add_u64 v[54:55], v[12:13], 0, s[10:11]
	v_lshl_add_u64 v[68:69], v[16:17], 0, s[10:11]
	s_lshl_b32 s10, s9, 1
	s_ashr_i32 s11, s10, 31
	s_lshl_b64 s[10:11], s[10:11], 10
	v_lshl_add_u64 v[70:71], v[18:19], 0, s[10:11]
	v_lshl_add_u64 v[76:77], v[20:21], 0, s[10:11]
	s_waitcnt vmcnt(8)
	v_mfma_f32_32x32x16_f16 a[0:15], v[84:87], v[6:9], a[0:15]
	ds_read_b128 v[104:107], v25
	v_mfma_f32_32x32x16_f16 a[0:15], v[84:87], v[2:5], a[0:15]
	ds_read_b128 v[108:111], v25 offset:12800
	v_mfma_f32_32x32x16_f16 a[16:31], v[124:127], v[2:5], a[16:31]
	ds_read_b128 v[100:103], v25 offset:2560
	v_mfma_f32_32x32x16_f16 a[16:31], v[88:91], v[6:9], a[16:31]
	ds_read_b128 v[96:99], v25 offset:15360
	v_mfma_f32_32x32x16_f16 a[16:31], v[88:91], v[2:5], a[16:31]
	ds_read_b128 v[92:95], v25 offset:5120
	v_mfma_f32_32x32x16_f16 a[32:47], v[128:131], v[2:5], a[32:47]
	ds_read_b128 v[88:91], v25 offset:17920
	v_mfma_f32_32x32x16_f16 a[32:47], v[132:135], v[6:9], a[32:47]
	ds_read_b128 v[84:87], v25 offset:7680
	v_mfma_f32_32x32x16_f16 a[32:47], v[132:135], v[2:5], a[32:47]
	global_load_dwordx4 v[68:71], v[70:71], off
	s_nop 0
	global_load_dwordx4 v[76:79], v[76:77], off
	v_mfma_f32_32x32x16_f16 a[48:63], v[136:139], v[2:5], a[48:63]
	v_mfma_f32_32x32x16_f16 a[48:63], v[116:119], v[6:9], a[48:63]
	v_mfma_f32_32x32x16_f16 a[48:63], v[116:119], v[2:5], a[48:63]
	s_add_i32 s2, s2, 2
	s_waitcnt lgkmcnt(0)
	s_waitcnt vmcnt(5)
	v_mfma_f32_32x32x16_f16 a[0:15], v[112:115], v[64:67], a[0:15]
	s_add_i32 s3, s2, -3
	s_min_i32 s3, s3, s8
	s_lshl_b32 s3, s3, 1
	ds_read_b128 v[116:119], v25 offset:10272
	s_or_b32 s10, s3, 1
	s_ashr_i32 s11, s10, 31
	s_lshl_b64 s[10:11], s[10:11], 10
	v_lshl_add_u64 v[2:3], v[18:19], 0, s[10:11]
	v_lshl_add_u64 v[6:7], v[20:21], 0, s[10:11]
	s_waitcnt vmcnt(4)
	v_mfma_f32_32x32x16_f16 a[0:15], v[104:107], v[80:83], a[0:15]
	ds_read_b128 v[112:115], v25 offset:32
	v_mfma_f32_32x32x16_f16 a[0:15], v[104:107], v[64:67], a[0:15]
	ds_read_b128 v[120:123], v25 offset:12832
	ds_write_b128 v26, v[44:47] offset:20480
	v_mfma_f32_32x32x16_f16 a[16:31], v[108:111], v[64:67], a[16:31]
	ds_read_b128 v[104:107], v25 offset:2592
	v_mfma_f32_32x32x16_f16 a[16:31], v[100:103], v[80:83], a[16:31]
	ds_read_b128 v[108:111], v25 offset:15392
	ds_write_b128 v26, v[48:51] offset:30720
	v_mfma_f32_32x32x16_f16 a[16:31], v[100:103], v[64:67], a[16:31]
	ds_read_b128 v[124:127], v25 offset:5152
	v_mfma_f32_32x32x16_f16 a[32:47], v[96:99], v[64:67], a[32:47]
	ds_read_b128 v[100:103], v25 offset:17952
	ds_write_b128 v26, v[32:35] offset:25600
	v_mfma_f32_32x32x16_f16 a[32:47], v[92:95], v[80:83], a[32:47]
	ds_read_b128 v[96:99], v25 offset:7712
	v_mfma_f32_32x32x16_f16 a[32:47], v[92:95], v[64:67], a[32:47]
	ds_write_b128 v26, v[28:31] offset:35840
	global_load_dwordx4 v[2:5], v[2:3], off
	s_nop 0
	global_load_dwordx4 v[6:9], v[6:7], off
	v_mfma_f32_32x32x16_f16 a[48:63], v[88:91], v[64:67], a[48:63]
	v_mfma_f32_32x32x16_f16 a[48:63], v[84:87], v[80:83], a[48:63]
	v_mfma_f32_32x32x16_f16 a[48:63], v[84:87], v[64:67], a[48:63]
	s_add_i32 s3, s2, -1
	s_min_i32 s9, s3, s8
	s_mul_i32 s10, s9, s25
	s_ashr_i32 s11, s10, 31
	s_lshl_b64 s[10:11], s[10:11], 1
	v_lshl_add_u64 v[28:29], v[14:15], 0, s[10:11]
	s_waitcnt lgkmcnt(0)
	s_barrier
	s_waitcnt vmcnt(5)
	v_mfma_f32_32x32x16_f16 a[0:15], v[116:119], v[36:39], a[0:15]
	s_add_i32 s3, s2, -2
	v_lshl_add_u64 v[28:29], v[10:11], 0, s[10:11]
	v_lshl_add_u64 v[30:31], v[12:13], 0, s[10:11]
	v_lshl_add_u64 v[64:65], v[16:17], 0, s[10:11]
	s_min_i32 s10, s3, s8
	ds_read_b128 v[84:87], v25 offset:30720
	s_lshl_b32 s10, s10, 1
	s_ashr_i32 s11, s10, 31
	s_lshl_b64 s[12:13], s[10:11], 10
	v_lshl_add_u64 v[66:67], v[18:19], 0, s[12:13]
	v_lshl_add_u64 v[80:81], v[20:21], 0, s[12:13]
	s_waitcnt vmcnt(4)
	v_mfma_f32_32x32x16_f16 a[0:15], v[112:115], v[40:43], a[0:15]
	ds_read_b128 v[88:91], v25 offset:20480
	v_mfma_f32_32x32x16_f16 a[0:15], v[112:115], v[36:39], a[0:15]
	ds_read_b128 v[92:95], v25 offset:33280
	v_mfma_f32_32x32x16_f16 a[16:31], v[120:123], v[36:39], a[16:31]
	ds_read_b128 v[112:115], v25 offset:23040
	v_mfma_f32_32x32x16_f16 a[16:31], v[104:107], v[40:43], a[16:31]
	ds_read_b128 v[116:119], v25 offset:35840
	v_mfma_f32_32x32x16_f16 a[16:31], v[104:107], v[36:39], a[16:31]
	ds_read_b128 v[120:123], v25 offset:25600
	v_mfma_f32_32x32x16_f16 a[32:47], v[108:111], v[36:39], a[32:47]
	ds_read_b128 v[104:107], v25 offset:38400
	v_mfma_f32_32x32x16_f16 a[32:47], v[124:127], v[40:43], a[32:47]
	ds_read_b128 v[108:111], v25 offset:28160
	v_mfma_f32_32x32x16_f16 a[32:47], v[124:127], v[36:39], a[32:47]
	v_mfma_f32_32x32x16_f16 a[48:63], v[100:103], v[36:39], a[48:63]
	v_mfma_f32_32x32x16_f16 a[48:63], v[96:99], v[40:43], a[48:63]
	v_mfma_f32_32x32x16_f16 a[48:63], v[96:99], v[36:39], a[48:63]
	s_waitcnt lgkmcnt(7)
	s_waitcnt vmcnt(3)
	v_mfma_f32_32x32x16_f16 a[0:15], v[84:87], v[68:71], a[0:15]
	ds_read_b128 v[96:99], v25 offset:30752
	s_or_b32 s10, s10, 1
	s_ashr_i32 s11, s10, 31
	s_lshl_b64 s[10:11], s[10:11], 10
	v_lshl_add_u64 v[36:37], v[18:19], 0, s[10:11]
	v_lshl_add_u64 v[40:41], v[20:21], 0, s[10:11]
	s_waitcnt lgkmcnt(7)
	s_waitcnt vmcnt(2)
	v_mfma_f32_32x32x16_f16 a[0:15], v[88:91], v[76:79], a[0:15]
	ds_read_b128 v[84:87], v25 offset:20512
	v_mfma_f32_32x32x16_f16 a[0:15], v[88:91], v[68:71], a[0:15]
	ds_read_b128 v[124:127], v25 offset:33312
	ds_write_b128 v26, v[60:63]
	s_waitcnt lgkmcnt(9)
	v_mfma_f32_32x32x16_f16 a[16:31], v[92:95], v[68:71], a[16:31]
	ds_read_b128 v[88:91], v25 offset:23072
	s_waitcnt lgkmcnt(9)
	v_mfma_f32_32x32x16_f16 a[16:31], v[112:115], v[76:79], a[16:31]
	ds_read_b128 v[128:131], v25 offset:35872
	ds_write_b128 v26, v[72:75] offset:10240
	v_mfma_f32_32x32x16_f16 a[16:31], v[112:115], v[68:71], a[16:31]
	ds_read_b128 v[132:135], v25 offset:25632
	s_waitcnt lgkmcnt(11)
	v_mfma_f32_32x32x16_f16 a[32:47], v[116:119], v[68:71], a[32:47]
	ds_read_b128 v[136:139], v25 offset:38432
	ds_write_b128 v26, v[56:59] offset:5120
	s_waitcnt lgkmcnt(12)
	v_mfma_f32_32x32x16_f16 a[32:47], v[120:123], v[76:79], a[32:47]
	ds_read_b128 v[116:119], v25 offset:28192
	v_mfma_f32_32x32x16_f16 a[32:47], v[120:123], v[68:71], a[32:47]
	ds_write_b128 v26, v[52:55] offset:15360
	s_waitcnt lgkmcnt(13)
	v_mfma_f32_32x32x16_f16 a[48:63], v[104:107], v[68:71], a[48:63]
	s_waitcnt lgkmcnt(12)
	v_mfma_f32_32x32x16_f16 a[48:63], v[108:111], v[76:79], a[48:63]
	v_mfma_f32_32x32x16_f16 a[48:63], v[108:111], v[68:71], a[48:63]
	s_min_i32 s10, s2, s8
	s_mul_i32 s10, s10, s25
	s_ashr_i32 s11, s10, 31
	s_lshl_b64 s[10:11], s[10:11], 1
	v_lshl_add_u64 v[52:53], v[14:15], 0, s[10:11]
	s_waitcnt lgkmcnt(0)
	s_barrier
	s_waitcnt vmcnt(1)
	v_mfma_f32_32x32x16_f16 a[0:15], v[96:99], v[2:5], a[0:15]
	ds_read_b128 v[112:115], v25 offset:10240
	v_lshl_add_u64 v[52:53], v[10:11], 0, s[10:11]
	v_lshl_add_u64 v[54:55], v[12:13], 0, s[10:11]
	v_lshl_add_u64 v[68:69], v[16:17], 0, s[10:11]
	s_lshl_b32 s10, s9, 1
	s_ashr_i32 s11, s10, 31
	s_lshl_b64 s[10:11], s[10:11], 10
	v_lshl_add_u64 v[70:71], v[18:19], 0, s[10:11]
	v_lshl_add_u64 v[76:77], v[20:21], 0, s[10:11]
	s_waitcnt vmcnt(0)
	v_mfma_f32_32x32x16_f16 a[0:15], v[84:87], v[6:9], a[0:15]
	ds_read_b128 v[104:107], v25
	v_mfma_f32_32x32x16_f16 a[0:15], v[84:87], v[2:5], a[0:15]
	ds_read_b128 v[108:111], v25 offset:12800
	v_mfma_f32_32x32x16_f16 a[16:31], v[124:127], v[2:5], a[16:31]
	ds_read_b128 v[100:103], v25 offset:2560
	v_mfma_f32_32x32x16_f16 a[16:31], v[88:91], v[6:9], a[16:31]
	ds_read_b128 v[96:99], v25 offset:15360
	v_mfma_f32_32x32x16_f16 a[16:31], v[88:91], v[2:5], a[16:31]
	ds_read_b128 v[92:95], v25 offset:5120
	v_mfma_f32_32x32x16_f16 a[32:47], v[128:131], v[2:5], a[32:47]
	ds_read_b128 v[88:91], v25 offset:17920
	v_mfma_f32_32x32x16_f16 a[32:47], v[132:135], v[6:9], a[32:47]
	ds_read_b128 v[84:87], v25 offset:7680
	v_mfma_f32_32x32x16_f16 a[32:47], v[132:135], v[2:5], a[32:47]
	v_mfma_f32_32x32x16_f16 a[48:63], v[136:139], v[2:5], a[48:63]
	v_mfma_f32_32x32x16_f16 a[48:63], v[116:119], v[6:9], a[48:63]
	v_mfma_f32_32x32x16_f16 a[48:63], v[116:119], v[2:5], a[48:63]
.LBB9_7:
	s_waitcnt vmcnt(0)
	s_load_dwordx4 s[0:3], s[0:1], 0x40
	s_ashr_i32 s4, s16, 31
	s_waitcnt vmcnt(1)
	v_lshlrev_b32_e32 v69, 5, v23
	v_lshl_or_b32 v70, s14, 7, v69
	v_mul_u32_u24_e32 v23, 0x2400, v23
	s_waitcnt lgkmcnt(0)
	s_mul_hi_u32 s8, s2, s16
	s_mul_i32 s4, s2, s4
	s_add_i32 s4, s8, s4
	s_mul_i32 s3, s3, s16
	s_add_i32 s3, s4, s3
	s_mul_i32 s2, s2, s16
	s_lshl_b64 s[2:3], s[2:3], 2
	s_add_u32 s4, s6, s2
	s_addc_u32 s6, s7, s3
	s_mul_hi_u32 s2, s0, s15
	s_mul_i32 s3, s0, s17
	s_add_i32 s2, s2, s3
	s_mul_i32 s3, s1, s15
	s_add_i32 s3, s2, s3
	s_mul_i32 s2, s0, s15
	s_lshl_b64 s[2:3], s[2:3], 2
	s_add_u32 s2, s4, s2
	s_addc_u32 s3, s6, s3
	v_ashrrev_i32_e32 v71, 31, v70
	v_lshlrev_b32_e32 v0, 4, v0
	v_accvgpr_read_b32 v68, a0
	v_accvgpr_read_b32 v67, a1
	v_lshl_add_u64 v[70:71], v[70:71], 2, s[2:3]
	v_and_b32_e32 v72, 0x70, v0
	v_mov_b32_e32 v73, 0
	v_lshl_or_b32 v22, v22, 2, v23
	s_movk_i32 s2, 0x240
	v_accvgpr_read_b32 v66, a2
	v_lshrrev_b32_e32 v69, 3, v1
	v_lshl_add_u64 v[0:1], v[70:71], 0, v[72:73]
	v_or_b32_e32 v70, v23, v72
	v_fma_f32 v23, s5, v68, 0
	v_mad_u32_u24 v68, v24, s2, v22
	v_fma_f32 v22, s5, v67, 0
	v_accvgpr_read_b32 v65, a3
	s_barrier
	ds_write_b32 v68, v22 offset:144
	v_fma_f32 v22, s5, v66, 0
	v_accvgpr_read_b32 v64, a4
	ds_write_b32 v68, v22 offset:288
	v_fma_f32 v22, s5, v65, 0
	v_accvgpr_read_b32 v63, a5
	ds_write_b32 v68, v22 offset:432
	v_fma_f32 v22, s5, v64, 0
	v_accvgpr_read_b32 v62, a6
	ds_write_b32 v68, v22 offset:1152
	v_fma_f32 v22, s5, v63, 0
	v_accvgpr_read_b32 v61, a7
	ds_write_b32 v68, v22 offset:1296
	v_fma_f32 v22, s5, v62, 0
	v_accvgpr_read_b32 v60, a8
	ds_write_b32 v68, v22 offset:1440
	v_fma_f32 v22, s5, v61, 0
	v_accvgpr_read_b32 v59, a9
	ds_write_b32 v68, v22 offset:1584
	v_fma_f32 v22, s5, v60, 0
	v_accvgpr_read_b32 v58, a10
	ds_write_b32 v68, v22 offset:2304
	v_fma_f32 v22, s5, v59, 0
	v_accvgpr_read_b32 v57, a11
	ds_write_b32 v68, v22 offset:2448
	v_fma_f32 v22, s5, v58, 0
	v_accvgpr_read_b32 v56, a12
	ds_write_b32 v68, v22 offset:2592
	v_fma_f32 v22, s5, v57, 0
	v_accvgpr_read_b32 v55, a13
	ds_write_b32 v68, v22 offset:2736
	v_fma_f32 v22, s5, v56, 0
	v_accvgpr_read_b32 v54, a14
	ds_write_b32 v68, v22 offset:3456
	v_fma_f32 v22, s5, v55, 0
	v_accvgpr_read_b32 v53, a15
	ds_write_b32 v68, v22 offset:3600
	v_fma_f32 v22, s5, v54, 0
	v_accvgpr_read_b32 v52, a16
	ds_write_b32 v68, v22 offset:3744
	v_fma_f32 v22, s5, v53, 0
	v_accvgpr_read_b32 v51, a17
	ds_write_b32 v68, v22 offset:3888
	v_fma_f32 v22, s5, v52, 0
	v_accvgpr_read_b32 v50, a18
	ds_write_b32 v68, v22 offset:4608
	v_fma_f32 v22, s5, v51, 0
	v_accvgpr_read_b32 v49, a19
	ds_write_b32 v68, v22 offset:4752
	v_fma_f32 v22, s5, v50, 0
	v_accvgpr_read_b32 v48, a20
	ds_write_b32 v68, v22 offset:4896
	v_fma_f32 v22, s5, v49, 0
	v_accvgpr_read_b32 v47, a21
	ds_write_b32 v68, v22 offset:5040
	v_fma_f32 v22, s5, v48, 0
	v_accvgpr_read_b32 v46, a22
	ds_write_b32 v68, v22 offset:5760
	v_fma_f32 v22, s5, v47, 0
	v_accvgpr_read_b32 v45, a23
	ds_write_b32 v68, v22 offset:5904
	v_fma_f32 v22, s5, v46, 0
	v_accvgpr_read_b32 v44, a24
	ds_write_b32 v68, v22 offset:6048
	v_fma_f32 v22, s5, v45, 0
	v_accvgpr_read_b32 v43, a25
	ds_write_b32 v68, v22 offset:6192
	v_fma_f32 v22, s5, v44, 0
	v_accvgpr_read_b32 v42, a26
	ds_write_b32 v68, v22 offset:6912
	v_fma_f32 v22, s5, v43, 0
	v_accvgpr_read_b32 v41, a27
	ds_write_b32 v68, v22 offset:7056
	v_fma_f32 v22, s5, v42, 0
	v_accvgpr_read_b32 v40, a28
	ds_write_b32 v68, v22 offset:7200
	v_fma_f32 v22, s5, v41, 0
	v_accvgpr_read_b32 v39, a29
	ds_write_b32 v68, v22 offset:7344
	v_fma_f32 v22, s5, v40, 0
	v_accvgpr_read_b32 v38, a30
	ds_write_b32 v68, v22 offset:8064
	v_fma_f32 v22, s5, v39, 0
	v_accvgpr_read_b32 v37, a31
	ds_write_b32 v68, v22 offset:8208
	v_fma_f32 v22, s5, v38, 0
	s_movk_i32 s4, 0x90
	ds_write_b32 v68, v22 offset:8352
	v_fma_f32 v22, s5, v37, 0
	v_mad_u32_u24 v71, v69, s4, v70
	ds_write_b32 v68, v23
	ds_write_b32 v68, v22 offset:8496
	ds_read_b128 v[38:41], v71
	v_mad_u64_u32 v[22:23], s[2:3], s0, v69, 0
	v_accvgpr_read_b32 v25, a43
	v_mov_b32_e32 v24, v23
	v_mad_u64_u32 v[42:43], s[2:3], s1, v69, v[24:25]
	v_mov_b32_e32 v23, v42
	v_or_b32_e32 v37, 8, v69
	v_lshl_add_u64 v[22:23], v[22:23], 2, v[0:1]
	v_mad_u32_u24 v46, v37, s4, v70
	ds_read_b128 v[42:45], v46
	s_waitcnt lgkmcnt(1)
	global_store_dwordx4 v[22:23], v[38:41], off sc1
	v_mad_u64_u32 v[22:23], s[2:3], s0, v37, 0
	v_mov_b32_e32 v24, v23
	v_mad_u64_u32 v[38:39], s[2:3], s1, v37, v[24:25]
	v_mov_b32_e32 v23, v38
	v_lshl_add_u64 v[22:23], v[22:23], 2, v[0:1]
	v_or_b32_e32 v37, 16, v69
	ds_read_b128 v[38:41], v46 offset:1152
	s_waitcnt lgkmcnt(1)
	global_store_dwordx4 v[22:23], v[42:45], off sc1
	v_mad_u64_u32 v[22:23], s[2:3], s0, v37, 0
	v_mov_b32_e32 v24, v23
	v_mad_u64_u32 v[42:43], s[2:3], s1, v37, v[24:25]
	v_mov_b32_e32 v23, v42
	v_lshl_add_u64 v[22:23], v[22:23], 2, v[0:1]
	v_or_b32_e32 v37, 24, v69
	ds_read_b128 v[42:45], v46 offset:2304
	s_waitcnt lgkmcnt(1)
	global_store_dwordx4 v[22:23], v[38:41], off sc1
	v_mad_u64_u32 v[22:23], s[2:3], s0, v37, 0
	v_mov_b32_e32 v24, v23
	v_mad_u64_u32 v[38:39], s[2:3], s1, v37, v[24:25]
	v_mov_b32_e32 v23, v38
	v_lshl_add_u64 v[22:23], v[22:23], 2, v[0:1]
	v_or_b32_e32 v37, 32, v69
	ds_read_b128 v[38:41], v46 offset:3456
	s_waitcnt lgkmcnt(1)
	global_store_dwordx4 v[22:23], v[42:45], off sc1
	v_mad_u64_u32 v[22:23], s[2:3], s0, v37, 0
	v_mov_b32_e32 v24, v23
	v_mad_u64_u32 v[42:43], s[2:3], s1, v37, v[24:25]
	v_mov_b32_e32 v23, v42
	v_lshl_add_u64 v[22:23], v[22:23], 2, v[0:1]
	v_or_b32_e32 v37, 40, v69
	ds_read_b128 v[42:45], v46 offset:4608
	s_waitcnt lgkmcnt(1)
	global_store_dwordx4 v[22:23], v[38:41], off sc1
	v_mad_u64_u32 v[22:23], s[2:3], s0, v37, 0
	v_mov_b32_e32 v24, v23
	v_mad_u64_u32 v[38:39], s[2:3], s1, v37, v[24:25]
	v_mov_b32_e32 v23, v38
	v_lshl_add_u64 v[22:23], v[22:23], 2, v[0:1]
	v_or_b32_e32 v37, 48, v69
	ds_read_b128 v[38:41], v46 offset:5760
	s_waitcnt lgkmcnt(1)
	global_store_dwordx4 v[22:23], v[42:45], off sc1
	v_mad_u64_u32 v[22:23], s[2:3], s0, v37, 0
	v_mov_b32_e32 v24, v23
	v_mad_u64_u32 v[42:43], s[2:3], s1, v37, v[24:25]
	v_mov_b32_e32 v23, v42
	v_lshl_add_u64 v[22:23], v[22:23], 2, v[0:1]
	v_or_b32_e32 v37, 56, v69
	ds_read_b128 v[42:45], v46 offset:6912
	s_waitcnt lgkmcnt(1)
	global_store_dwordx4 v[22:23], v[38:41], off sc1
	v_mad_u64_u32 v[22:23], s[2:3], s0, v37, 0
	v_mov_b32_e32 v24, v23
	v_mad_u64_u32 v[38:39], s[2:3], s1, v37, v[24:25]
	v_mov_b32_e32 v23, v38
	v_accvgpr_read_b32 v36, a32
	v_lshl_add_u64 v[22:23], v[22:23], 2, v[0:1]
	v_accvgpr_read_b32 v35, a33
	s_waitcnt lgkmcnt(0)
	global_store_dwordx4 v[22:23], v[42:45], off sc1
	v_fma_f32 v22, s5, v36, 0
	v_accvgpr_read_b32 v34, a34
	ds_write_b32 v68, v22
	v_fma_f32 v22, s5, v35, 0
	v_accvgpr_read_b32 v33, a35
	ds_write_b32 v68, v22 offset:144
	v_fma_f32 v22, s5, v34, 0
	v_accvgpr_read_b32 v32, a36
	ds_write_b32 v68, v22 offset:288
	v_fma_f32 v22, s5, v33, 0
	v_accvgpr_read_b32 v31, a37
	ds_write_b32 v68, v22 offset:432
	v_fma_f32 v22, s5, v32, 0
	v_accvgpr_read_b32 v30, a38
	ds_write_b32 v68, v22 offset:1152
	v_fma_f32 v22, s5, v31, 0
	v_accvgpr_read_b32 v29, a39
	ds_write_b32 v68, v22 offset:1296
	v_fma_f32 v22, s5, v30, 0
	v_accvgpr_read_b32 v28, a40
	ds_write_b32 v68, v22 offset:1440
	v_fma_f32 v22, s5, v29, 0
	v_accvgpr_read_b32 v27, a41
	ds_write_b32 v68, v22 offset:1584
	v_fma_f32 v22, s5, v28, 0
	v_accvgpr_read_b32 v26, a42
	ds_write_b32 v68, v22 offset:2304
	v_fma_f32 v22, s5, v27, 0
	v_accvgpr_read_b32 v17, a48
	v_accvgpr_read_b32 v16, a49
	v_accvgpr_read_b32 v15, a50
	v_accvgpr_read_b32 v14, a51
	v_accvgpr_read_b32 v13, a52
	v_accvgpr_read_b32 v12, a53
	v_accvgpr_read_b32 v11, a54
	v_accvgpr_read_b32 v10, a55
	v_accvgpr_read_b32 v9, a56
	v_accvgpr_read_b32 v8, a57
	v_accvgpr_read_b32 v7, a58
	v_accvgpr_read_b32 v6, a59
	v_accvgpr_read_b32 v5, a60
	v_accvgpr_read_b32 v4, a61
	v_accvgpr_read_b32 v3, a62
	v_accvgpr_read_b32 v2, a63
	v_accvgpr_read_b32 v21, a44
	v_accvgpr_read_b32 v20, a45
	v_accvgpr_read_b32 v19, a46
	v_accvgpr_read_b32 v18, a47
	ds_write_b32 v68, v22 offset:2448
	v_fma_f32 v22, s5, v26, 0
	ds_write_b32 v68, v22 offset:2592
	v_fma_f32 v22, s5, v25, 0
	v_fma_f32 v21, s5, v21, 0
	v_fma_f32 v20, s5, v20, 0
	v_fma_f32 v19, s5, v19, 0
	v_fma_f32 v18, s5, v18, 0
	v_fma_f32 v17, s5, v17, 0
	v_fma_f32 v16, s5, v16, 0
	v_fma_f32 v15, s5, v15, 0
	v_fma_f32 v14, s5, v14, 0
	v_fma_f32 v13, s5, v13, 0
	v_fma_f32 v12, s5, v12, 0
	v_fma_f32 v11, s5, v11, 0
	v_fma_f32 v10, s5, v10, 0
	v_fma_f32 v9, s5, v9, 0
	v_fma_f32 v8, s5, v8, 0
	v_fma_f32 v7, s5, v7, 0
	v_fma_f32 v6, s5, v6, 0
	v_fma_f32 v5, s5, v5, 0
	v_fma_f32 v4, s5, v4, 0
	v_fma_f32 v3, s5, v3, 0
	v_fma_f32 v2, s5, v2, 0
	ds_write_b32 v68, v22 offset:2736
	ds_write_b32 v68, v21 offset:3456
	ds_write_b32 v68, v20 offset:3600
	ds_write_b32 v68, v19 offset:3744
	ds_write_b32 v68, v18 offset:3888
	ds_write_b32 v68, v17 offset:4608
	ds_write_b32 v68, v16 offset:4752
	ds_write_b32 v68, v15 offset:4896
	ds_write_b32 v68, v14 offset:5040
	ds_write_b32 v68, v13 offset:5760
	ds_write_b32 v68, v12 offset:5904
	ds_write_b32 v68, v11 offset:6048
	ds_write_b32 v68, v10 offset:6192
	ds_write_b32 v68, v9 offset:6912
	ds_write_b32 v68, v8 offset:7056
	ds_write_b32 v68, v7 offset:7200
	ds_write_b32 v68, v6 offset:7344
	ds_write_b32 v68, v5 offset:8064
	ds_write_b32 v68, v4 offset:8208
	ds_write_b32 v68, v3 offset:8352
	ds_write_b32 v68, v2 offset:8496
	v_or_b32_e32 v9, 64, v69
	ds_read_b128 v[2:5], v71
	v_mad_u64_u32 v[6:7], s[2:3], s0, v9, 0
	v_mov_b32_e32 v8, v7
	v_mad_u64_u32 v[8:9], s[2:3], s1, v9, v[8:9]
	v_mov_b32_e32 v7, v8
	v_lshl_add_u64 v[10:11], v[6:7], 2, v[0:1]
	ds_read_b128 v[6:9], v46
	s_waitcnt lgkmcnt(1)
	global_store_dwordx4 v[10:11], v[2:5], off sc1
	s_nop 1
	v_or_b32_e32 v5, 0x48, v69
	v_mad_u64_u32 v[2:3], s[2:3], s0, v5, 0
	v_mov_b32_e32 v4, v3
	v_mad_u64_u32 v[4:5], s[2:3], s1, v5, v[4:5]
	v_mov_b32_e32 v3, v4
	v_lshl_add_u64 v[2:3], v[2:3], 2, v[0:1]
	s_waitcnt lgkmcnt(0)
	global_store_dwordx4 v[2:3], v[6:9], off sc1
	ds_read_b128 v[2:5], v46 offset:1152
	s_nop 0
	v_or_b32_e32 v9, 0x50, v69
	v_mad_u64_u32 v[6:7], s[2:3], s0, v9, 0
	v_mov_b32_e32 v8, v7
	v_mad_u64_u32 v[8:9], s[2:3], s1, v9, v[8:9]
	v_mov_b32_e32 v7, v8
	v_lshl_add_u64 v[10:11], v[6:7], 2, v[0:1]
	ds_read_b128 v[6:9], v46 offset:2304
	s_waitcnt lgkmcnt(1)
	global_store_dwordx4 v[10:11], v[2:5], off sc1
	s_nop 1
	v_or_b32_e32 v5, 0x58, v69
	v_mad_u64_u32 v[2:3], s[2:3], s0, v5, 0
	v_mov_b32_e32 v4, v3
	v_mad_u64_u32 v[4:5], s[2:3], s1, v5, v[4:5]
	v_mov_b32_e32 v3, v4
	v_lshl_add_u64 v[2:3], v[2:3], 2, v[0:1]
	s_waitcnt lgkmcnt(0)
	global_store_dwordx4 v[2:3], v[6:9], off sc1
	ds_read_b128 v[2:5], v46 offset:3456
	s_nop 0
	v_or_b32_e32 v9, 0x60, v69
	v_mad_u64_u32 v[6:7], s[2:3], s0, v9, 0
	v_mov_b32_e32 v8, v7
	v_mad_u64_u32 v[8:9], s[2:3], s1, v9, v[8:9]
	v_mov_b32_e32 v7, v8
	v_lshl_add_u64 v[10:11], v[6:7], 2, v[0:1]
	ds_read_b128 v[6:9], v46 offset:4608
	s_waitcnt lgkmcnt(1)
	global_store_dwordx4 v[10:11], v[2:5], off sc1
	s_nop 1
	v_or_b32_e32 v5, 0x68, v69
	v_mad_u64_u32 v[2:3], s[2:3], s0, v5, 0
	v_mov_b32_e32 v4, v3
	v_mad_u64_u32 v[4:5], s[2:3], s1, v5, v[4:5]
	v_mov_b32_e32 v3, v4
	v_lshl_add_u64 v[2:3], v[2:3], 2, v[0:1]
	s_waitcnt lgkmcnt(0)
	global_store_dwordx4 v[2:3], v[6:9], off sc1
	ds_read_b128 v[2:5], v46 offset:5760
	s_nop 0
	v_or_b32_e32 v9, 0x70, v69
	v_mad_u64_u32 v[6:7], s[2:3], s0, v9, 0
	v_mov_b32_e32 v8, v7
	v_mad_u64_u32 v[8:9], s[2:3], s1, v9, v[8:9]
	v_mov_b32_e32 v7, v8
	v_lshl_add_u64 v[10:11], v[6:7], 2, v[0:1]
	ds_read_b128 v[6:9], v46 offset:6912
	s_waitcnt lgkmcnt(1)
	global_store_dwordx4 v[10:11], v[2:5], off sc1
	s_nop 1
	v_or_b32_e32 v5, 0x78, v69
	v_mad_u64_u32 v[2:3], s[2:3], s0, v5, 0
	v_mov_b32_e32 v4, v3
	v_mad_u64_u32 v[4:5], s[0:1], s1, v5, v[4:5]
	v_mov_b32_e32 v3, v4
	v_lshl_add_u64 v[0:1], v[2:3], 2, v[0:1]
	s_waitcnt lgkmcnt(0)
	global_store_dwordx4 v[0:1], v[6:9], off sc1
	s_endpgm
	s_endpgm
	s_endpgm
	s_endpgm
	s_endpgm
	s_endpgm
	s_endpgm
	s_endpgm
	s_endpgm
	s_endpgm
	s_endpgm
	s_endpgm
	s_endpgm
	s_endpgm
	s_endpgm
	s_endpgm
	s_endpgm
	s_endpgm
	s_endpgm
	s_endpgm
	s_endpgm
	s_endpgm
	s_endpgm
	s_endpgm
	s_endpgm
	s_endpgm
	s_endpgm
	s_endpgm
	s_endpgm
	s_endpgm
	s_endpgm
	s_endpgm
	s_endpgm
	s_endpgm
	s_endpgm
	s_endpgm

.LBB10_4:
	s_load_dwordx4 s[32:35], s[0:1], 0x18
	s_load_dword s36, s[0:1], 0x28
	s_load_dwordx4 s[4:7], s[0:1], 0x60
	s_load_dwordx2 s[12:13], s[0:1], 0x10
	s_ashr_i32 s2, s2, 3
	s_add_i32 s2, s3, s2
	s_abs_i32 s3, s2
	s_waitcnt lgkmcnt(0)
	s_lshl_b32 s26, s7, 6
	s_lshl_b32 s24, s26, 5
	s_mov_b32 s27, 0
	s_cmp_eq_u32 s12, 0x800
	s_cselect_b32 s25, s24, 32
	s_cselect_b32 s26, s26, 1
	s_cselect_b32 s12, 32, s12
	s_mov_b32 s92, s6
	s_mov_b32 s93, s7
	v_cvt_f32_u32_e32 v72, s6
	v_cvt_f32_u32_e32 v73, s7
	v_cvt_f32_u32_e32 v74, s2
	v_rcp_iflag_f32_e32 v72, v72
	v_rcp_iflag_f32_e32 v73, v73
	v_add_f32_e32 v74, 0.5, v74
	s_nop 0
	v_mul_f32_e32 v74, v74, v72
	v_cvt_u32_f32_e32 v74, v74
	v_cvt_f32_u32_e32 v72, v74
	v_add_f32_e32 v72, 0.5, v72
	v_readfirstlane_b32 s94, v74
	v_mul_f32_e32 v72, v72, v73
	v_cvt_u32_f32_e32 v72, v72
	s_mul_i32 s90, s94, s92
	s_sub_i32 s90, s2, s90
	v_readfirstlane_b32 s95, v72
	s_nop 0
	s_mul_i32 s91, s95, s93
	s_sub_i32 s91, s94, s91
	s_mov_b32 s3, s94
	s_mov_b32 s14, s90
	s_mov_b32 s16, s95
	s_mov_b32 s2, s91
	v_lshlrev_b32_e32 v2, 3, v0
	v_lshrrev_b32_e32 v13, 2, v0
	v_and_b32_e32 v14, 24, v2
	v_mov_b32_e32 v15, 0
	v_lshrrev_b32_e32 v11, 6, v0
	v_and_b32_e32 v10, 31, v0
	s_lshl_b32 s15, s2, 6
	s_mul_i32 s2, s16, s4
	s_mul_i32 s26, s2, s26
	s_ashr_i32 s3, s2, 31
	v_or_b32_e32 v1, s15, v13
	s_ashr_i32 s17, s15, 31
	v_lshl_add_u64 v[2:3], s[26:27], 0, v[14:15]
	s_mul_i32 s18, s12, s17
	v_mad_u64_u32 v[2:3], s[6:7], s12, v1, v[2:3]
	v_mul_lo_u32 v1, s13, v1
	v_add3_u32 v3, v1, v3, s18
	v_lshlrev_b64 v[4:5], 1, v[2:3]
	v_lshl_add_u64 v[2:3], s[10:11], 0, v[4:5]
	v_lshl_add_u64 v[4:5], s[8:9], 0, v[4:5]
	global_load_dwordx4 v[76:79], v[4:5], off
	global_load_dwordx4 v[88:91], v[2:3], off
	s_load_dwordx2 s[6:7], s[0:1], 0x38
	s_movk_i32 s9, 0x50
	v_lshlrev_b32_e32 v14, 1, v14
	v_and_b32_e32 v1, 63, v0
	s_nop 7
	v_bfe_u32 v12, v0, 5, 1
	v_mad_u32_u24 v15, v13, s9, v14
	s_mov_b32 s10, s36
	s_lshr_b32 s3, s3, 28
	s_add_i32 s2, s2, s3
	s_ashr_i32 s2, s2, 4
	s_ashr_i32 s8, s4, 31
	s_waitcnt lgkmcnt(0)
	s_ashr_i32 s12, s10, 31
	s_lshr_b32 s12, s12, 28
	s_add_i32 s10, s10, s12
	s_ashr_i32 s3, s2, 31
	s_lshr_b32 s8, s8, 27
	v_lshl_or_b32 v8, s14, 2, v11
	s_ashr_i32 s10, s10, 4
	v_mov_b32_e32 v6, s2
	v_mov_b32_e32 v7, s3
	s_add_i32 s4, s4, s8
	v_mad_i64_i32 v[6:7], s[2:3], v8, s10, v[6:7]
	s_ashr_i32 s4, s4, 5
	v_lshlrev_b64 v[8:9], 10, v[6:7]
	s_add_i32 s8, s4, -1
	v_lshl_or_b32 v8, v1, 4, v8
	s_min_i32 s11, s8, 2
	v_lshl_add_u64 v[6:7], s[32:33], 0, v[8:9]
	s_lshl_b32 s28, s25, 1
	s_mov_b32 s29, 0
	v_lshl_add_u64 v[72:73], v[4:5], 0, s[28:29]
	v_lshl_add_u64 v[74:75], v[2:3], 0, s[28:29]
	global_load_dwordx4 v[28:31], v[72:73], off
	global_load_dwordx4 v[20:23], v[74:75], off
	v_lshl_add_u64 v[8:9], s[34:35], 0, v[8:9]
	global_load_dwordx4 v[36:39], v[6:7], off
	global_load_dwordx4 v[16:19], v[6:7], off offset:1024
	global_load_dwordx4 v[52:55], v[8:9], off
	global_load_dwordx4 v[24:27], v[8:9], off offset:1024
	global_load_dwordx4 v[40:43], v[6:7], off offset:2048
	global_load_dwordx4 v[48:51], v[8:9], off offset:2048
	s_mul_i32 s2, s11, s25
	s_ashr_i32 s3, s2, 31
	s_lshl_b64 s[2:3], s[2:3], 1
	v_lshl_add_u64 v[58:59], v[4:5], 0, s[2:3]
	v_lshl_add_u64 v[56:57], v[2:3], 0, s[2:3]
	global_load_dwordx4 v[44:47], v[58:59], off
	global_load_dwordx4 v[32:35], v[56:57], off
	v_accvgpr_write_b32 a0, 0
	v_accvgpr_write_b32 a1, 0
	v_accvgpr_write_b32 a2, 0
	v_accvgpr_write_b32 a3, 0
	v_accvgpr_write_b32 a4, 0
	v_accvgpr_write_b32 a5, 0
	v_accvgpr_write_b32 a6, 0
	v_accvgpr_write_b32 a7, 0
	v_accvgpr_write_b32 a8, 0
	v_accvgpr_write_b32 a9, 0
	v_accvgpr_write_b32 a10, 0
	v_accvgpr_write_b32 a11, 0
	v_accvgpr_write_b32 a12, 0
	v_accvgpr_write_b32 a13, 0
	v_accvgpr_write_b32 a14, 0
	v_accvgpr_write_b32 a15, 0
	v_accvgpr_write_b32 a16, 0
	v_accvgpr_write_b32 a17, 0
	v_accvgpr_write_b32 a18, 0
	v_accvgpr_write_b32 a19, 0
	v_accvgpr_write_b32 a20, 0
	v_accvgpr_write_b32 a21, 0
	v_accvgpr_write_b32 a22, 0
	v_accvgpr_write_b32 a23, 0
	v_accvgpr_write_b32 a24, 0
	v_accvgpr_write_b32 a25, 0
	v_accvgpr_write_b32 a26, 0
	v_accvgpr_write_b32 a27, 0
	v_accvgpr_write_b32 a28, 0
	v_accvgpr_write_b32 a29, 0
	v_accvgpr_write_b32 a30, 0
	v_accvgpr_write_b32 a31, 0
	s_waitcnt vmcnt(11)
	ds_write_b128 v15, v[76:79]
	s_waitcnt vmcnt(10)
	ds_write_b128 v15, v[88:91] offset:5120
	s_waitcnt lgkmcnt(0)
	s_barrier
	v_mul_u32_u24_e32 v15, 0x50, v13
	v_lshlrev_b32_e32 v13, 4, v12
	v_mad_u32_u24 v68, v10, s9, v13
	ds_read_b128 v[56:59], v68 offset:2560
	ds_read_b128 v[64:67], v68
	ds_read_b128 v[60:63], v68 offset:7680
	ds_read_b128 v[68:71], v68 offset:5120
	v_mul_u32_u24_e32 v72, 0x50, v10
	s_mov_b32 s2, 4
	s_nop 7
	v_add_u32_e32 v13, v13, v72
	v_add_u32_e32 v14, v14, v15
	s_add_i32 s3, s4, -2
	s_cmp_gt_i32 s2, s3
	s_cbranch_scc1 .Ltail_LBB10
.LBB10_6:
	s_waitcnt vmcnt(7) lgkmcnt(0)
	v_mfma_f32_32x32x16_f16 a[0:15], v[68:71], v[36:39], a[0:15]
	s_add_i32 s3, s2, -3
	s_min_i32 s3, s3, s8
	s_lshl_b32 s3, s3, 1
	ds_read_b128 v[72:75], v13 offset:5152
	s_or_b32 s10, s3, 1
	s_ashr_i32 s11, s10, 31
	s_lshl_b64 s[10:11], s[10:11], 10
	v_lshl_add_u64 v[88:89], v[6:7], 0, s[10:11]
	v_lshl_add_u64 v[90:91], v[8:9], 0, s[10:11]
	s_waitcnt vmcnt(5)
	v_mfma_f32_32x32x16_f16 a[0:15], v[64:67], v[52:55], a[0:15]
	ds_read_b128 v[68:71], v13 offset:32
	v_mfma_f32_32x32x16_f16 a[0:15], v[64:67], v[36:39], a[0:15]
	ds_read_b128 v[76:79], v13 offset:7712
	ds_write_b128 v14, v[28:31] offset:10240
	global_load_dwordx4 v[80:83], v[88:89], off
	global_load_dwordx4 v[84:87], v[90:91], off
	v_mfma_f32_32x32x16_f16 a[16:31], v[60:63], v[36:39], a[16:31]
	ds_read_b128 v[64:67], v13 offset:2592
	ds_write_b128 v14, v[20:23] offset:15360
	v_mfma_f32_32x32x16_f16 a[16:31], v[56:59], v[52:55], a[16:31]
	v_mfma_f32_32x32x16_f16 a[16:31], v[56:59], v[36:39], a[16:31]
	s_add_i32 s3, s2, -1
	s_min_i32 s3, s3, s8
	s_mul_i32 s10, s3, s25
	s_ashr_i32 s11, s10, 31
	s_lshl_b64 s[10:11], s[10:11], 1
	v_lshl_add_u64 v[20:21], v[4:5], 0, s[10:11]
	s_waitcnt lgkmcnt(0)
	s_barrier
	global_load_dwordx4 v[28:31], v[20:21], off
	v_mfma_f32_32x32x16_f16 a[0:15], v[72:75], v[16:19], a[0:15]
	s_add_i32 s9, s2, -2
	ds_read_b128 v[56:59], v13 offset:15360
	v_lshl_add_u64 v[20:21], v[2:3], 0, s[10:11]
	s_min_i32 s10, s9, s8
	s_lshl_b32 s10, s10, 1
	s_ashr_i32 s11, s10, 31
	s_lshl_b64 s[12:13], s[10:11], 10
	v_lshl_add_u64 v[88:89], v[6:7], 0, s[12:13]
	v_lshl_add_u64 v[90:91], v[8:9], 0, s[12:13]
	global_load_dwordx4 v[20:23], v[20:21], off
	s_waitcnt vmcnt(8)
	v_mfma_f32_32x32x16_f16 a[0:15], v[68:71], v[24:27], a[0:15]
	ds_read_b128 v[60:63], v13 offset:10240
	v_mfma_f32_32x32x16_f16 a[0:15], v[68:71], v[16:19], a[0:15]
	ds_read_b128 v[72:75], v13 offset:17920
	global_load_dwordx4 v[36:39], v[88:89], off
	global_load_dwordx4 v[52:55], v[90:91], off
	v_mfma_f32_32x32x16_f16 a[16:31], v[76:79], v[16:19], a[16:31]
	ds_read_b128 v[68:71], v13 offset:12800
	v_mfma_f32_32x32x16_f16 a[16:31], v[64:67], v[24:27], a[16:31]
	v_mfma_f32_32x32x16_f16 a[16:31], v[64:67], v[16:19], a[16:31]
	s_waitcnt vmcnt(7) lgkmcnt(3)
	v_mfma_f32_32x32x16_f16 a[0:15], v[56:59], v[40:43], a[0:15]
	ds_read_b128 v[64:67], v13 offset:15392
	s_or_b32 s10, s10, 1
	s_ashr_i32 s11, s10, 31
	s_lshl_b64 s[10:11], s[10:11], 10
	v_lshl_add_u64 v[88:89], v[6:7], 0, s[10:11]
	v_lshl_add_u64 v[90:91], v[8:9], 0, s[10:11]
	s_waitcnt vmcnt(6) lgkmcnt(3)
	v_mfma_f32_32x32x16_f16 a[0:15], v[60:63], v[48:51], a[0:15]
	ds_read_b128 v[56:59], v13 offset:10272
	v_mfma_f32_32x32x16_f16 a[0:15], v[60:63], v[40:43], a[0:15]
	ds_read_b128 v[76:79], v13 offset:17952
	s_waitcnt vmcnt(7)
	ds_write_b128 v14, v[44:47]
	global_load_dwordx4 v[16:19], v[88:89], off
	global_load_dwordx4 v[24:27], v[90:91], off
	s_waitcnt lgkmcnt(5)
	v_mfma_f32_32x32x16_f16 a[16:31], v[72:75], v[40:43], a[16:31]
	ds_read_b128 v[88:91], v13 offset:12832
	s_waitcnt vmcnt(8)
	ds_write_b128 v14, v[32:35] offset:5120
	s_waitcnt lgkmcnt(6)
	v_mfma_f32_32x32x16_f16 a[16:31], v[68:71], v[48:51], a[16:31]
	v_mfma_f32_32x32x16_f16 a[16:31], v[68:71], v[40:43], a[16:31]
	s_min_i32 s10, s2, s8
	s_mul_i32 s10, s10, s25
	s_ashr_i32 s11, s10, 31
	s_lshl_b64 s[10:11], s[10:11], 1
	v_lshl_add_u64 v[32:33], v[4:5], 0, s[10:11]
	s_waitcnt lgkmcnt(0)
	s_barrier
	global_load_dwordx4 v[44:47], v[32:33], off
	s_waitcnt vmcnt(8)
	v_mfma_f32_32x32x16_f16 a[0:15], v[64:67], v[80:83], a[0:15]
	ds_read_b128 v[68:71], v13 offset:5120
	v_lshl_add_u64 v[32:33], v[2:3], 0, s[10:11]
	s_lshl_b32 s10, s3, 1
	s_ashr_i32 s11, s10, 31
	s_lshl_b64 s[10:11], s[10:11], 10
	v_lshl_add_u64 v[72:73], v[6:7], 0, s[10:11]
	v_lshl_add_u64 v[74:75], v[8:9], 0, s[10:11]
	global_load_dwordx4 v[32:35], v[32:33], off
	s_waitcnt vmcnt(8)
	v_mfma_f32_32x32x16_f16 a[0:15], v[56:59], v[84:87], a[0:15]
	ds_read_b128 v[64:67], v13
	v_mfma_f32_32x32x16_f16 a[0:15], v[56:59], v[80:83], a[0:15]
	ds_read_b128 v[60:63], v13 offset:7680
	global_load_dwordx4 v[40:43], v[72:73], off
	global_load_dwordx4 v[48:51], v[74:75], off
	v_mfma_f32_32x32x16_f16 a[16:31], v[76:79], v[80:83], a[16:31]
	ds_read_b128 v[56:59], v13 offset:2560
	v_mfma_f32_32x32x16_f16 a[16:31], v[88:91], v[84:87], a[16:31]
	v_mfma_f32_32x32x16_f16 a[16:31], v[88:91], v[80:83], a[16:31]
	s_add_i32 s2, s2, 2
	s_add_i32 s3, s4, -2
	s_cmp_le_i32 s2, s3
	s_cbranch_scc1 .LBB10_6
.Ltail_LBB10:
	s_waitcnt lgkmcnt(0)
	s_waitcnt vmcnt(7)
	v_mfma_f32_32x32x16_f16 a[0:15], v[68:71], v[36:39], a[0:15]
	s_add_i32 s3, s2, -3
	s_min_i32 s3, s3, s8
	s_lshl_b32 s3, s3, 1
	ds_read_b128 v[72:75], v13 offset:5152
	s_or_b32 s10, s3, 1
	s_ashr_i32 s11, s10, 31
	s_lshl_b64 s[10:11], s[10:11], 10
	v_lshl_add_u64 v[88:89], v[6:7], 0, s[10:11]
	v_lshl_add_u64 v[90:91], v[8:9], 0, s[10:11]
	s_waitcnt vmcnt(5)
	v_mfma_f32_32x32x16_f16 a[0:15], v[64:67], v[52:55], a[0:15]
	ds_read_b128 v[68:71], v13 offset:32
	v_mfma_f32_32x32x16_f16 a[0:15], v[64:67], v[36:39], a[0:15]
	ds_read_b128 v[76:79], v13 offset:7712
	ds_write_b128 v14, v[28:31] offset:10240
	global_load_dwordx4 v[80:83], v[88:89], off
	global_load_dwordx4 v[84:87], v[90:91], off
	v_mfma_f32_32x32x16_f16 a[16:31], v[60:63], v[36:39], a[16:31]
	ds_read_b128 v[64:67], v13 offset:2592
	ds_write_b128 v14, v[20:23] offset:15360
	v_mfma_f32_32x32x16_f16 a[16:31], v[56:59], v[52:55], a[16:31]
	v_mfma_f32_32x32x16_f16 a[16:31], v[56:59], v[36:39], a[16:31]
	s_add_i32 s3, s2, -1
	s_min_i32 s3, s3, s8
	s_mul_i32 s10, s3, s25
	s_ashr_i32 s11, s10, 31
	s_lshl_b64 s[10:11], s[10:11], 1
	v_lshl_add_u64 v[20:21], v[4:5], 0, s[10:11]
	s_waitcnt lgkmcnt(0)
	s_barrier
	global_load_dwordx4 v[28:31], v[20:21], off
	v_mfma_f32_32x32x16_f16 a[0:15], v[72:75], v[16:19], a[0:15]
	s_add_i32 s9, s2, -2
	ds_read_b128 v[56:59], v13 offset:15360
	v_lshl_add_u64 v[20:21], v[2:3], 0, s[10:11]
	s_min_i32 s10, s9, s8
	s_lshl_b32 s10, s10, 1
	s_ashr_i32 s11, s10, 31
	s_lshl_b64 s[12:13], s[10:11], 10
	v_lshl_add_u64 v[88:89], v[6:7], 0, s[12:13]
	v_lshl_add_u64 v[90:91], v[8:9], 0, s[12:13]
	global_load_dwordx4 v[20:23], v[20:21], off
	s_waitcnt vmcnt(8)
	v_mfma_f32_32x32x16_f16 a[0:15], v[68:71], v[24:27], a[0:15]
	ds_read_b128 v[60:63], v13 offset:10240
	v_mfma_f32_32x32x16_f16 a[0:15], v[68:71], v[16:19], a[0:15]
	ds_read_b128 v[72:75], v13 offset:17920
	global_load_dwordx4 v[36:39], v[88:89], off
	global_load_dwordx4 v[52:55], v[90:91], off
	v_mfma_f32_32x32x16_f16 a[16:31], v[76:79], v[16:19], a[16:31]
	ds_read_b128 v[68:71], v13 offset:12800
	v_mfma_f32_32x32x16_f16 a[16:31], v[64:67], v[24:27], a[16:31]
	v_mfma_f32_32x32x16_f16 a[16:31], v[64:67], v[16:19], a[16:31]
	s_waitcnt lgkmcnt(3)
	s_waitcnt vmcnt(7)
	v_mfma_f32_32x32x16_f16 a[0:15], v[56:59], v[40:43], a[0:15]
	ds_read_b128 v[64:67], v13 offset:15392
	s_or_b32 s10, s10, 1
	s_ashr_i32 s11, s10, 31
	s_lshl_b64 s[10:11], s[10:11], 10
	v_lshl_add_u64 v[88:89], v[6:7], 0, s[10:11]
	v_lshl_add_u64 v[90:91], v[8:9], 0, s[10:11]
	s_waitcnt lgkmcnt(3)
	s_waitcnt vmcnt(6)
	v_mfma_f32_32x32x16_f16 a[0:15], v[60:63], v[48:51], a[0:15]
	ds_read_b128 v[56:59], v13 offset:10272
	v_mfma_f32_32x32x16_f16 a[0:15], v[60:63], v[40:43], a[0:15]
	ds_read_b128 v[76:79], v13 offset:17952
	s_waitcnt vmcnt(7)
	ds_write_b128 v14, v[44:47]
	global_load_dwordx4 v[16:19], v[88:89], off
	global_load_dwordx4 v[24:27], v[90:91], off
	s_waitcnt lgkmcnt(5)
	v_mfma_f32_32x32x16_f16 a[16:31], v[72:75], v[40:43], a[16:31]
	ds_read_b128 v[88:91], v13 offset:12832
	s_waitcnt vmcnt(8)
	ds_write_b128 v14, v[32:35] offset:5120
	s_waitcnt lgkmcnt(6)
	v_mfma_f32_32x32x16_f16 a[16:31], v[68:71], v[48:51], a[16:31]
	v_mfma_f32_32x32x16_f16 a[16:31], v[68:71], v[40:43], a[16:31]
	s_min_i32 s10, s2, s8
	s_mul_i32 s10, s10, s25
	s_ashr_i32 s11, s10, 31
	s_lshl_b64 s[10:11], s[10:11], 1
	v_lshl_add_u64 v[32:33], v[4:5], 0, s[10:11]
	s_waitcnt lgkmcnt(0)
	s_barrier
	s_waitcnt vmcnt(7)
	v_mfma_f32_32x32x16_f16 a[0:15], v[64:67], v[80:83], a[0:15]
	ds_read_b128 v[68:71], v13 offset:5120
	v_lshl_add_u64 v[32:33], v[2:3], 0, s[10:11]
	s_lshl_b32 s10, s3, 1
	s_ashr_i32 s11, s10, 31
	s_lshl_b64 s[10:11], s[10:11], 10
	v_lshl_add_u64 v[72:73], v[6:7], 0, s[10:11]
	v_lshl_add_u64 v[74:75], v[8:9], 0, s[10:11]
	s_waitcnt vmcnt(6)
	v_mfma_f32_32x32x16_f16 a[0:15], v[56:59], v[84:87], a[0:15]
	ds_read_b128 v[64:67], v13
	v_mfma_f32_32x32x16_f16 a[0:15], v[56:59], v[80:83], a[0:15]
	ds_read_b128 v[60:63], v13 offset:7680
	global_load_dwordx4 v[40:43], v[72:73], off
	global_load_dwordx4 v[48:51], v[74:75], off
	v_mfma_f32_32x32x16_f16 a[16:31], v[76:79], v[80:83], a[16:31]
	ds_read_b128 v[56:59], v13 offset:2560
	v_mfma_f32_32x32x16_f16 a[16:31], v[88:91], v[84:87], a[16:31]
	v_mfma_f32_32x32x16_f16 a[16:31], v[88:91], v[80:83], a[16:31]
	s_add_i32 s2, s2, 2
	s_waitcnt lgkmcnt(0)
	s_waitcnt vmcnt(5)
	v_mfma_f32_32x32x16_f16 a[0:15], v[68:71], v[36:39], a[0:15]
	s_add_i32 s3, s2, -3
	s_min_i32 s3, s3, s8
	s_lshl_b32 s3, s3, 1
	ds_read_b128 v[72:75], v13 offset:5152
	s_or_b32 s10, s3, 1
	s_ashr_i32 s11, s10, 31
	s_lshl_b64 s[10:11], s[10:11], 10
	v_lshl_add_u64 v[88:89], v[6:7], 0, s[10:11]
	v_lshl_add_u64 v[90:91], v[8:9], 0, s[10:11]
	s_waitcnt vmcnt(4)
	v_mfma_f32_32x32x16_f16 a[0:15], v[64:67], v[52:55], a[0:15]
	ds_read_b128 v[68:71], v13 offset:32
	v_mfma_f32_32x32x16_f16 a[0:15], v[64:67], v[36:39], a[0:15]
	ds_read_b128 v[76:79], v13 offset:7712
	ds_write_b128 v14, v[28:31] offset:10240
	global_load_dwordx4 v[80:83], v[88:89], off
	global_load_dwordx4 v[84:87], v[90:91], off
	v_mfma_f32_32x32x16_f16 a[16:31], v[60:63], v[36:39], a[16:31]
	ds_read_b128 v[64:67], v13 offset:2592
	ds_write_b128 v14, v[20:23] offset:15360
	v_mfma_f32_32x32x16_f16 a[16:31], v[56:59], v[52:55], a[16:31]
	v_mfma_f32_32x32x16_f16 a[16:31], v[56:59], v[36:39], a[16:31]
	s_add_i32 s3, s2, -1
	s_min_i32 s3, s3, s8
	s_mul_i32 s10, s3, s25
	s_ashr_i32 s11, s10, 31
	s_lshl_b64 s[10:11], s[10:11], 1
	v_lshl_add_u64 v[20:21], v[4:5], 0, s[10:11]
	s_waitcnt lgkmcnt(0)
	s_barrier
	s_waitcnt vmcnt(5)
	v_mfma_f32_32x32x16_f16 a[0:15], v[72:75], v[16:19], a[0:15]
	s_add_i32 s9, s2, -2
	ds_read_b128 v[56:59], v13 offset:15360
	v_lshl_add_u64 v[20:21], v[2:3], 0, s[10:11]
	s_min_i32 s10, s9, s8
	s_lshl_b32 s10, s10, 1
	s_ashr_i32 s11, s10, 31
	s_lshl_b64 s[12:13], s[10:11], 10
	v_lshl_add_u64 v[88:89], v[6:7], 0, s[12:13]
	v_lshl_add_u64 v[90:91], v[8:9], 0, s[12:13]
	s_waitcnt vmcnt(4)
	v_mfma_f32_32x32x16_f16 a[0:15], v[68:71], v[24:27], a[0:15]
	ds_read_b128 v[60:63], v13 offset:10240
	v_mfma_f32_32x32x16_f16 a[0:15], v[68:71], v[16:19], a[0:15]
	ds_read_b128 v[72:75], v13 offset:17920
	v_mfma_f32_32x32x16_f16 a[16:31], v[76:79], v[16:19], a[16:31]
	ds_read_b128 v[68:71], v13 offset:12800
	v_mfma_f32_32x32x16_f16 a[16:31], v[64:67], v[24:27], a[16:31]
	v_mfma_f32_32x32x16_f16 a[16:31], v[64:67], v[16:19], a[16:31]
	s_waitcnt lgkmcnt(3)
	s_waitcnt vmcnt(3)
	v_mfma_f32_32x32x16_f16 a[0:15], v[56:59], v[40:43], a[0:15]
	ds_read_b128 v[64:67], v13 offset:15392
	s_or_b32 s10, s10, 1
	s_ashr_i32 s11, s10, 31
	s_lshl_b64 s[10:11], s[10:11], 10
	v_lshl_add_u64 v[88:89], v[6:7], 0, s[10:11]
	v_lshl_add_u64 v[90:91], v[8:9], 0, s[10:11]
	s_waitcnt lgkmcnt(3)
	s_waitcnt vmcnt(2)
	v_mfma_f32_32x32x16_f16 a[0:15], v[60:63], v[48:51], a[0:15]
	ds_read_b128 v[56:59], v13 offset:10272
	v_mfma_f32_32x32x16_f16 a[0:15], v[60:63], v[40:43], a[0:15]
	ds_read_b128 v[76:79], v13 offset:17952
	ds_write_b128 v14, v[44:47]
	s_waitcnt lgkmcnt(5)
	v_mfma_f32_32x32x16_f16 a[16:31], v[72:75], v[40:43], a[16:31]
	ds_read_b128 v[88:91], v13 offset:12832
	ds_write_b128 v14, v[32:35] offset:5120
	s_waitcnt lgkmcnt(6)
	v_mfma_f32_32x32x16_f16 a[16:31], v[68:71], v[48:51], a[16:31]
	v_mfma_f32_32x32x16_f16 a[16:31], v[68:71], v[40:43], a[16:31]
	s_min_i32 s10, s2, s8
	s_mul_i32 s10, s10, s25
	s_ashr_i32 s11, s10, 31
	s_lshl_b64 s[10:11], s[10:11], 1
	v_lshl_add_u64 v[32:33], v[4:5], 0, s[10:11]
	s_waitcnt lgkmcnt(0)
	s_barrier
	s_waitcnt vmcnt(1)
	v_mfma_f32_32x32x16_f16 a[0:15], v[64:67], v[80:83], a[0:15]
	ds_read_b128 v[68:71], v13 offset:5120
	v_lshl_add_u64 v[32:33], v[2:3], 0, s[10:11]
	s_lshl_b32 s10, s3, 1
	s_ashr_i32 s11, s10, 31
	s_lshl_b64 s[10:11], s[10:11], 10
	v_lshl_add_u64 v[72:73], v[6:7], 0, s[10:11]
	v_lshl_add_u64 v[74:75], v[8:9], 0, s[10:11]
	s_waitcnt vmcnt(0)
	v_mfma_f32_32x32x16_f16 a[0:15], v[56:59], v[84:87], a[0:15]
	ds_read_b128 v[64:67], v13
	v_mfma_f32_32x32x16_f16 a[0:15], v[56:59], v[80:83], a[0:15]
	ds_read_b128 v[60:63], v13 offset:7680
	v_mfma_f32_32x32x16_f16 a[16:31], v[76:79], v[80:83], a[16:31]
	ds_read_b128 v[56:59], v13 offset:2560
	v_mfma_f32_32x32x16_f16 a[16:31], v[88:91], v[84:87], a[16:31]
	v_mfma_f32_32x32x16_f16 a[16:31], v[88:91], v[80:83], a[16:31]
.LBB10_7:
	s_waitcnt vmcnt(0)
	s_load_dwordx4 s[0:3], s[0:1], 0x40
	s_ashr_i32 s4, s16, 31
	s_waitcnt vmcnt(7)
	v_lshlrev_b32_e32 v37, 5, v11
	v_lshl_or_b32 v38, s14, 7, v37
	v_mul_u32_u24_e32 v37, 0x2400, v11
	s_waitcnt lgkmcnt(0)
	s_mul_hi_u32 s8, s2, s16
	s_mul_i32 s4, s2, s4
	s_add_i32 s4, s8, s4
	s_mul_i32 s3, s3, s16
	s_add_i32 s3, s4, s3
	s_mul_hi_u32 s4, s0, s15
	s_mul_i32 s8, s0, s17
	s_add_i32 s4, s4, s8
	s_mul_i32 s8, s1, s15
	v_accvgpr_read_b32 v36, a0
	s_waitcnt vmcnt(2)
	v_accvgpr_read_b32 v35, a1
	s_add_i32 s9, s4, s8
	v_lshl_or_b32 v10, v10, 2, v37
	s_movk_i32 s4, 0x240
	v_accvgpr_read_b32 v34, a2
	v_accvgpr_read_b32 v33, a3
	v_fma_f32 v36, s5, v36, 0
	v_mad_u32_u24 v10, v12, s4, v10
	v_fma_f32 v12, s5, v35, 0
	v_accvgpr_read_b32 v32, a4
	v_accvgpr_read_b32 v31, a5
	s_barrier
	ds_write2_b32 v10, v36, v12 offset1:36
	v_fma_f32 v12, s5, v34, 0
	v_fma_f32 v33, s5, v33, 0
	v_accvgpr_read_b32 v30, a6
	v_accvgpr_read_b32 v29, a7
	ds_write2_b32 v10, v12, v33 offset0:72 offset1:108
	v_fma_f32 v12, s5, v32, 0
	v_fma_f32 v31, s5, v31, 0
	v_add_u32_e32 v32, 0x400, v10
	v_accvgpr_read_b32 v28, a8
	v_accvgpr_read_b32 v27, a9
	ds_write2_b32 v32, v12, v31 offset0:32 offset1:68
	v_fma_f32 v12, s5, v30, 0
	v_fma_f32 v29, s5, v29, 0
	v_accvgpr_read_b32 v26, a10
	v_accvgpr_read_b32 v25, a11
	ds_write2_b32 v32, v12, v29 offset0:104 offset1:140
	v_fma_f32 v12, s5, v28, 0
	v_fma_f32 v27, s5, v27, 0
	v_add_u32_e32 v28, 0x800, v10
	v_accvgpr_read_b32 v24, a12
	v_accvgpr_read_b32 v23, a13
	ds_write2_b32 v28, v12, v27 offset0:64 offset1:100
	v_fma_f32 v12, s5, v26, 0
	v_fma_f32 v25, s5, v25, 0
	v_accvgpr_read_b32 v22, a14
	v_accvgpr_read_b32 v21, a15
	ds_write2_b32 v28, v12, v25 offset0:136 offset1:172
	v_fma_f32 v12, s5, v24, 0
	v_fma_f32 v23, s5, v23, 0
	v_add_u32_e32 v24, 0xc00, v10
	v_accvgpr_read_b32 v20, a16
	v_accvgpr_read_b32 v19, a17
	ds_write2_b32 v24, v12, v23 offset0:96 offset1:132
	v_fma_f32 v12, s5, v22, 0
	v_fma_f32 v21, s5, v21, 0
	v_accvgpr_read_b32 v18, a18
	v_accvgpr_read_b32 v17, a19
	ds_write2_b32 v24, v12, v21 offset0:168 offset1:204
	v_fma_f32 v12, s5, v20, 0
	v_fma_f32 v19, s5, v19, 0
	v_add_u32_e32 v20, 0x1000, v10
	v_accvgpr_read_b32 v16, a20
	v_accvgpr_read_b32 v15, a21
	ds_write2_b32 v20, v12, v19 offset0:128 offset1:164
	v_fma_f32 v12, s5, v18, 0
	v_fma_f32 v17, s5, v17, 0
	v_accvgpr_read_b32 v14, a22
	v_accvgpr_read_b32 v13, a23
	s_mul_i32 s2, s2, s16
	ds_write2_b32 v20, v12, v17 offset0:200 offset1:236
	v_fma_f32 v12, s5, v16, 0
	v_fma_f32 v15, s5, v15, 0
	v_add_u32_e32 v16, 0x1400, v10
	v_accvgpr_read_b32 v9, a24
	v_accvgpr_read_b32 v8, a25
	ds_write2_b32 v16, v12, v15 offset0:160 offset1:196
	v_fma_f32 v12, s5, v14, 0
	v_fma_f32 v13, s5, v13, 0
	v_add_u32_e32 v14, 0x1600, v10
	s_lshl_b64 s[2:3], s[2:3], 2
	v_accvgpr_read_b32 v7, a26
	v_accvgpr_read_b32 v6, a27
	v_accvgpr_read_b32 v5, a28
	v_accvgpr_read_b32 v4, a29
	v_accvgpr_read_b32 v3, a30
	v_accvgpr_read_b32 v2, a31
	s_mul_i32 s8, s0, s15
	ds_write2_b32 v14, v12, v13 offset0:104 offset1:140
	v_fma_f32 v9, s5, v9, 0
	v_fma_f32 v8, s5, v8, 0
	v_add_u32_e32 v12, 0x1800, v10
	s_add_u32 s4, s6, s2
	ds_write2_b32 v12, v9, v8 offset0:192 offset1:228
	v_fma_f32 v7, s5, v7, 0
	v_fma_f32 v6, s5, v6, 0
	v_add_u32_e32 v8, 0x1c00, v10
	v_fma_f32 v5, s5, v5, 0
	v_fma_f32 v4, s5, v4, 0
	v_fma_f32 v3, s5, v3, 0
	v_fma_f32 v2, s5, v2, 0
	s_addc_u32 s5, s7, s3
	s_lshl_b64 s[2:3], s[8:9], 2
	ds_write2_b32 v8, v7, v6 offset0:8 offset1:44
	v_add_u32_e32 v6, 0x1e00, v10
	s_add_u32 s2, s4, s2
	v_lshlrev_b32_e32 v0, 4, v0
	v_ashrrev_i32_e32 v39, 31, v38
	ds_write2_b32 v6, v5, v4 offset0:96 offset1:132
	v_add_u32_e32 v4, 0x2000, v10
	s_addc_u32 s3, s5, s3
	v_and_b32_e32 v10, 0x70, v0
	ds_write2_b32 v4, v3, v2 offset0:40 offset1:76
	v_lshrrev_b32_e32 v12, 3, v1
	v_lshl_add_u64 v[2:3], v[38:39], 2, s[2:3]
	v_or_b32_e32 v0, v37, v10
	s_movk_i32 s2, 0x90
	v_mov_b32_e32 v11, 0
	v_mad_u32_u24 v13, v12, s2, v0
	v_lshl_add_u64 v[8:9], v[2:3], 0, v[10:11]
	ds_read_b128 v[0:3], v13
	v_mad_u64_u32 v[4:5], s[2:3], s0, v12, 0
	v_mov_b32_e32 v6, v5
	v_mad_u64_u32 v[6:7], s[2:3], s1, v12, v[6:7]
	v_mov_b32_e32 v5, v6
	v_lshl_add_u64 v[10:11], v[4:5], 2, v[8:9]
	ds_read_b128 v[4:7], v13 offset:1152
	s_waitcnt lgkmcnt(1)
	global_store_dwordx4 v[10:11], v[0:3], off sc1
	s_nop 1
	v_or_b32_e32 v3, 8, v12
	v_mad_u64_u32 v[0:1], s[2:3], s0, v3, 0
	v_mov_b32_e32 v2, v1
	v_mad_u64_u32 v[2:3], s[2:3], s1, v3, v[2:3]
	v_mov_b32_e32 v1, v2
	v_lshl_add_u64 v[0:1], v[0:1], 2, v[8:9]
	s_waitcnt lgkmcnt(0)
	global_store_dwordx4 v[0:1], v[4:7], off sc1
	ds_read_b128 v[0:3], v13 offset:2304
	s_nop 0
	v_or_b32_e32 v7, 16, v12
	v_mad_u64_u32 v[4:5], s[2:3], s0, v7, 0
	v_mov_b32_e32 v6, v5
	v_mad_u64_u32 v[6:7], s[2:3], s1, v7, v[6:7]
	v_mov_b32_e32 v5, v6
	v_lshl_add_u64 v[10:11], v[4:5], 2, v[8:9]
	ds_read_b128 v[4:7], v13 offset:3456
	s_waitcnt lgkmcnt(1)
	global_store_dwordx4 v[10:11], v[0:3], off sc1
	s_nop 1
	v_or_b32_e32 v3, 24, v12
	v_mad_u64_u32 v[0:1], s[2:3], s0, v3, 0
	v_mov_b32_e32 v2, v1
	v_mad_u64_u32 v[2:3], s[2:3], s1, v3, v[2:3]
	v_mov_b32_e32 v1, v2
	v_lshl_add_u64 v[0:1], v[0:1], 2, v[8:9]
	s_waitcnt lgkmcnt(0)
	global_store_dwordx4 v[0:1], v[4:7], off sc1
	ds_read_b128 v[0:3], v13 offset:4608
	s_nop 0
	v_or_b32_e32 v7, 32, v12
	v_mad_u64_u32 v[4:5], s[2:3], s0, v7, 0
	v_mov_b32_e32 v6, v5
	v_mad_u64_u32 v[6:7], s[2:3], s1, v7, v[6:7]
	v_mov_b32_e32 v5, v6
	v_lshl_add_u64 v[10:11], v[4:5], 2, v[8:9]
	ds_read_b128 v[4:7], v13 offset:5760
	s_waitcnt lgkmcnt(1)
	global_store_dwordx4 v[10:11], v[0:3], off sc1
	s_nop 1
	v_or_b32_e32 v3, 40, v12
	v_mad_u64_u32 v[0:1], s[2:3], s0, v3, 0
	v_mov_b32_e32 v2, v1
	v_mad_u64_u32 v[2:3], s[2:3], s1, v3, v[2:3]
	v_mov_b32_e32 v1, v2
	v_lshl_add_u64 v[0:1], v[0:1], 2, v[8:9]
	s_waitcnt lgkmcnt(0)
	global_store_dwordx4 v[0:1], v[4:7], off sc1
	ds_read_b128 v[0:3], v13 offset:6912
	s_nop 0
	v_or_b32_e32 v7, 48, v12
	v_mad_u64_u32 v[4:5], s[2:3], s0, v7, 0
	v_mov_b32_e32 v6, v5
	v_mad_u64_u32 v[6:7], s[2:3], s1, v7, v[6:7]
	v_mov_b32_e32 v5, v6
	v_lshl_add_u64 v[10:11], v[4:5], 2, v[8:9]
	ds_read_b128 v[4:7], v13 offset:8064
	s_waitcnt lgkmcnt(1)
	global_store_dwordx4 v[10:11], v[0:3], off sc1
	s_nop 1
	v_or_b32_e32 v3, 56, v12
	v_mad_u64_u32 v[0:1], s[2:3], s0, v3, 0
	v_mov_b32_e32 v2, v1
	v_mad_u64_u32 v[2:3], s[0:1], s1, v3, v[2:3]
	v_mov_b32_e32 v1, v2
	v_lshl_add_u64 v[0:1], v[0:1], 2, v[8:9]
	s_waitcnt lgkmcnt(0)
	global_store_dwordx4 v[0:1], v[4:7], off sc1
	s_endpgm
	s_endpgm
	s_endpgm
	s_endpgm
	s_endpgm
	s_endpgm
	s_endpgm
	s_endpgm
	s_endpgm
	s_endpgm
	s_endpgm
	s_endpgm
	s_endpgm
	s_endpgm
	s_endpgm
	s_endpgm
	s_endpgm
	s_endpgm
	s_endpgm
	s_endpgm
	s_endpgm
	s_endpgm
	s_endpgm

.LBB16_4:
	s_load_dwordx4 s[32:35], s[0:1], 0x18
	s_load_dword s36, s[0:1], 0x28
	s_load_dwordx4 s[4:7], s[0:1], 0x60
	s_load_dwordx2 s[14:15], s[0:1], 0x10
	s_ashr_i32 s2, s2, 3
	s_add_i32 s2, s3, s2
	s_abs_i32 s3, s2
	s_waitcnt lgkmcnt(0)
	s_mov_b32 s92, s6
	s_mov_b32 s93, s7
	v_cvt_f32_u32_e32 v100, s6
	v_cvt_f32_u32_e32 v101, s7
	v_cvt_f32_u32_e32 v102, s2
	v_rcp_iflag_f32_e32 v100, v100
	v_rcp_iflag_f32_e32 v101, v101
	v_add_f32_e32 v102, 0.5, v102
	s_nop 0
	v_mul_f32_e32 v102, v102, v100
	v_cvt_u32_f32_e32 v102, v102
	v_cvt_f32_u32_e32 v100, v102
	v_add_f32_e32 v100, 0.5, v100
	v_readfirstlane_b32 s94, v102
	v_mul_f32_e32 v100, v100, v101
	v_cvt_u32_f32_e32 v100, v100
	s_mul_i32 s90, s94, s92
	s_sub_i32 s90, s2, s90
	v_readfirstlane_b32 s95, v100
	s_nop 0
	s_mul_i32 s91, s95, s93
	s_sub_i32 s91, s94, s91
	s_mov_b32 s3, s94
	s_mov_b32 s16, s90
	s_mov_b32 s2, s95
	s_mov_b32 s3, s91
	v_lshrrev_b32_e32 v11, 6, v0
	v_mov_b32_e32 v9, 0
	v_lshlrev_b32_e32 v6, 5, v11
	v_and_b32_e32 v24, 31, v0
	v_and_b32_e32 v25, 63, v0
	v_bfe_u32 v26, v0, 5, 1
	v_lshrrev_b32_e32 v1, 2, v0
	v_lshlrev_b32_e32 v2, 3, v0
	s_mul_i32 s2, s2, s4
	s_lshl_b32 s6, s3, 7
	v_and_b32_e32 v8, 24, v2
	s_ashr_i32 s3, s2, 31
	v_or_b32_e32 v4, s6, v1
	s_ashr_i32 s7, s6, 31
	v_lshl_add_u64 v[2:3], s[2:3], 0, v[8:9]
	s_mul_i32 s17, s14, s7
	v_mad_u64_u32 v[2:3], s[20:21], s14, v4, v[2:3]
	v_mul_lo_u32 v4, s15, v4
	v_lshl_or_b32 v10, s16, 7, v6
	s_lshl_b64 s[18:19], s[14:15], 6
	v_add3_u32 v3, v4, v3, s17
	v_or_b32_e32 v6, v10, v24
	v_lshl_add_u64 v[4:5], v[2:3], 0, s[18:19]
	v_lshlrev_b64 v[2:3], 1, v[2:3]
	v_ashrrev_i32_e32 v7, 31, v6
	v_lshl_add_u64 v[12:13], v[4:5], 1, s[10:11]
	v_lshl_add_u64 v[14:15], s[12:13], 0, v[2:3]
	v_lshl_add_u64 v[16:17], s[10:11], 0, v[2:3]
	s_lshl_b64 s[10:11], s[14:15], 7
	v_lshl_add_u64 v[6:7], v[6:7], 2, s[8:9]
	v_lshl_add_u64 v[18:19], v[14:15], 0, s[10:11]
	global_load_dwordx4 v[126:129], v[16:17], off
	global_load_dwordx4 v[130:133], v[14:15], off
	global_load_dwordx4 v[134:137], v[12:13], off
	global_load_dwordx4 v[138:141], v[18:19], off
	global_load_dword v9, v[6:7], off
	v_lshlrev_b32_e32 v0, 1, v8
	s_movk_i32 s9, 0x50
	s_nop 7
	v_mad_u32_u24 v118, v1, s9, v0
	s_mov_b32 s10, s36
	s_lshr_b32 s3, s3, 28
	s_ashr_i32 s8, s4, 31
	v_lshl_or_b32 v4, s16, 2, v11
	s_add_i32 s2, s2, s3
	s_waitcnt lgkmcnt(0)
	s_ashr_i32 s16, s10, 31
	s_lshr_b32 s8, s8, 27
	s_lshr_b32 s16, s16, 28
	s_ashr_i32 s2, s2, 4
	s_add_i32 s4, s4, s8
	s_add_i32 s10, s10, s16
	s_ashr_i32 s3, s2, 31
	s_ashr_i32 s4, s4, 5
	s_ashr_i32 s10, s10, 4
	v_mov_b32_e32 v2, s2
	v_mov_b32_e32 v3, s3
	s_add_i32 s8, s4, -1
	v_mad_i64_i32 v[2:3], s[2:3], v4, s10, v[2:3]
	s_min_i32 s11, s8, 2
	v_lshlrev_b64 v[2:3], 10, v[2:3]
	v_lshl_or_b32 v2, v25, 4, v2
	s_lshl_b32 s2, s11, 5
	v_lshl_add_u64 v[20:21], s[32:33], 0, v[2:3]
	s_ashr_i32 s3, s2, 31
	global_load_dwordx4 v[46:49], v[16:17], off offset:64
	global_load_dwordx4 v[50:53], v[14:15], off offset:64
	global_load_dwordx4 v[34:37], v[12:13], off offset:64
	global_load_dwordx4 v[30:33], v[18:19], off offset:64
	v_lshl_add_u64 v[22:23], s[34:35], 0, v[2:3]
	global_load_dwordx4 v[66:69], v[20:21], off
	global_load_dwordx4 v[38:41], v[20:21], off offset:1024
	global_load_dwordx4 v[82:85], v[22:23], off
	global_load_dwordx4 v[42:45], v[22:23], off offset:1024
	global_load_dwordx4 v[70:73], v[20:21], off offset:2048
	global_load_dwordx4 v[78:81], v[22:23], off offset:2048
	s_lshl_b64 s[2:3], s[2:3], 1
	v_lshl_add_u64 v[28:29], v[16:17], 0, s[2:3]
	v_lshl_add_u64 v[2:3], v[12:13], 0, s[2:3]
	v_lshl_add_u64 v[4:5], v[14:15], 0, s[2:3]
	v_lshl_add_u64 v[6:7], v[18:19], 0, s[2:3]
	global_load_dwordx4 v[62:65], v[28:29], off
	global_load_dwordx4 v[58:61], v[2:3], off
	global_load_dwordx4 v[74:77], v[4:5], off
	global_load_dwordx4 v[54:57], v[6:7], off
	v_accvgpr_write_b32 a48, 0
	v_accvgpr_write_b32 a49, 0
	v_accvgpr_write_b32 a50, 0
	v_accvgpr_write_b32 a51, 0
	v_accvgpr_write_b32 a52, 0
	v_accvgpr_write_b32 a53, 0
	v_accvgpr_write_b32 a54, 0
	v_accvgpr_write_b32 a55, 0
	v_accvgpr_write_b32 a56, 0
	v_accvgpr_write_b32 a57, 0
	v_accvgpr_write_b32 a58, 0
	v_accvgpr_write_b32 a59, 0
	v_accvgpr_write_b32 a60, 0
	v_accvgpr_write_b32 a61, 0
	v_accvgpr_write_b32 a62, 0
	v_accvgpr_write_b32 a63, 0
	v_accvgpr_write_b32 a32, 0
	v_accvgpr_write_b32 a33, 0
	v_accvgpr_write_b32 a34, 0
	v_accvgpr_write_b32 a35, 0
	v_accvgpr_write_b32 a36, 0
	v_accvgpr_write_b32 a37, 0
	v_accvgpr_write_b32 a38, 0
	v_accvgpr_write_b32 a39, 0
	v_accvgpr_write_b32 a40, 0
	v_accvgpr_write_b32 a41, 0
	v_accvgpr_write_b32 a42, 0
	v_accvgpr_write_b32 a43, 0
	v_accvgpr_write_b32 a44, 0
	v_accvgpr_write_b32 a45, 0
	v_accvgpr_write_b32 a46, 0
	v_accvgpr_write_b32 a47, 0
	v_accvgpr_write_b32 a16, 0
	v_accvgpr_write_b32 a17, 0
	v_accvgpr_write_b32 a18, 0
	v_accvgpr_write_b32 a19, 0
	v_accvgpr_write_b32 a20, 0
	v_accvgpr_write_b32 a21, 0
	v_accvgpr_write_b32 a22, 0
	v_accvgpr_write_b32 a23, 0
	v_accvgpr_write_b32 a24, 0
	v_accvgpr_write_b32 a25, 0
	v_accvgpr_write_b32 a26, 0
	v_accvgpr_write_b32 a27, 0
	v_accvgpr_write_b32 a28, 0
	v_accvgpr_write_b32 a29, 0
	v_accvgpr_write_b32 a30, 0
	v_accvgpr_write_b32 a31, 0
	v_accvgpr_write_b32 a0, 0
	v_accvgpr_write_b32 a1, 0
	v_accvgpr_write_b32 a2, 0
	v_accvgpr_write_b32 a3, 0
	v_accvgpr_write_b32 a4, 0
	v_accvgpr_write_b32 a5, 0
	v_accvgpr_write_b32 a6, 0
	v_accvgpr_write_b32 a7, 0
	v_accvgpr_write_b32 a8, 0
	v_accvgpr_write_b32 a9, 0
	v_accvgpr_write_b32 a10, 0
	v_accvgpr_write_b32 a11, 0
	v_accvgpr_write_b32 a12, 0
	v_accvgpr_write_b32 a13, 0
	v_accvgpr_write_b32 a14, 0
	v_accvgpr_write_b32 a15, 0
	s_waitcnt vmcnt(18)
	ds_write_b128 v118, v[126:129]
	s_waitcnt vmcnt(17)
	ds_write_b128 v118, v[130:133] offset:10240
	s_waitcnt vmcnt(16)
	ds_write_b128 v118, v[134:137] offset:5120
	s_waitcnt vmcnt(15)
	ds_write_b128 v118, v[138:141] offset:15360
	s_waitcnt lgkmcnt(0)
	s_barrier
	v_lshlrev_b32_e32 v2, 4, v26
	v_mad_u32_u24 v4, v24, s9, v2
	ds_read_b128 v[86:89], v4 offset:7680
	ds_read_b128 v[94:97], v4 offset:5120
	ds_read_b128 v[90:93], v4 offset:17920
	ds_read_b128 v[98:101], v4 offset:15360
	ds_read_b128 v[102:105], v4 offset:2560
	ds_read_b128 v[106:109], v4
	ds_read_b128 v[110:113], v4 offset:12800
	ds_read_b128 v[114:117], v4 offset:10240
	v_mul_u32_u24_e32 v1, 0x50, v1
	v_mul_u32_u24_e32 v3, 0x50, v24
	s_mov_b32 s2, 4
	s_nop 7
	v_add_u32_e32 v27, v2, v3
	v_add_u32_e32 v28, v0, v1
	s_add_i32 s3, s4, -2
	s_cmp_gt_i32 s2, s3
	s_cbranch_scc1 .Ltail_LBB16
.LBB16_6:
	s_waitcnt vmcnt(9) lgkmcnt(0)
	v_mfma_f32_32x32x16_f16 a[0:15], v[114:117], v[66:69], a[0:15]
	s_add_i32 s3, s2, -3
	s_min_i32 s3, s3, s8
	s_lshl_b32 s3, s3, 1
	ds_read_b128 v[118:121], v27 offset:10272
	s_or_b32 s10, s3, 1
	s_ashr_i32 s11, s10, 31
	s_lshl_b64 s[10:11], s[10:11], 10
	v_lshl_add_u64 v[0:1], v[20:21], 0, s[10:11]
	v_lshl_add_u64 v[4:5], v[22:23], 0, s[10:11]
	s_waitcnt vmcnt(7)
	v_mfma_f32_32x32x16_f16 a[0:15], v[106:109], v[82:85], a[0:15]
	ds_read_b128 v[114:117], v27 offset:32
	v_mfma_f32_32x32x16_f16 a[0:15], v[106:109], v[66:69], a[0:15]
	ds_read_b128 v[122:125], v27 offset:12832
	ds_write_b128 v28, v[46:49] offset:20480
	v_mfma_f32_32x32x16_f16 a[16:31], v[110:113], v[66:69], a[16:31]
	ds_read_b128 v[106:109], v27 offset:2592
	v_mfma_f32_32x32x16_f16 a[16:31], v[102:105], v[82:85], a[16:31]
	ds_read_b128 v[110:113], v27 offset:15392
	ds_write_b128 v28, v[50:53] offset:30720
	v_mfma_f32_32x32x16_f16 a[16:31], v[102:105], v[66:69], a[16:31]
	ds_read_b128 v[126:129], v27 offset:5152
	v_mfma_f32_32x32x16_f16 a[32:47], v[98:101], v[66:69], a[32:47]
	ds_read_b128 v[102:105], v27 offset:17952
	ds_write_b128 v28, v[34:37] offset:25600
	v_mfma_f32_32x32x16_f16 a[32:47], v[94:97], v[82:85], a[32:47]
	ds_read_b128 v[98:101], v27 offset:7712
	v_mfma_f32_32x32x16_f16 a[32:47], v[94:97], v[66:69], a[32:47]
	ds_write_b128 v28, v[30:33] offset:35840
	global_load_dwordx4 v[0:3], v[0:1], off
	s_nop 0
	global_load_dwordx4 v[4:7], v[4:5], off
	v_mfma_f32_32x32x16_f16 a[48:63], v[90:93], v[66:69], a[48:63]
	v_mfma_f32_32x32x16_f16 a[48:63], v[86:89], v[82:85], a[48:63]
	v_mfma_f32_32x32x16_f16 a[48:63], v[86:89], v[66:69], a[48:63]
	s_add_i32 s3, s2, -1
	s_min_i32 s9, s3, s8
	s_lshl_b32 s10, s9, 5
	s_ashr_i32 s11, s10, 31
	s_lshl_b64 s[10:11], s[10:11], 1
	v_lshl_add_u64 v[30:31], v[16:17], 0, s[10:11]
	s_waitcnt lgkmcnt(0)
	s_barrier
	global_load_dwordx4 v[46:49], v[30:31], off
	v_mfma_f32_32x32x16_f16 a[0:15], v[118:121], v[38:41], a[0:15]
	s_add_i32 s3, s2, -2
	v_lshl_add_u64 v[30:31], v[12:13], 0, s[10:11]
	v_lshl_add_u64 v[32:33], v[14:15], 0, s[10:11]
	v_lshl_add_u64 v[66:67], v[18:19], 0, s[10:11]
	s_min_i32 s10, s3, s8
	ds_read_b128 v[86:89], v27 offset:30720
	s_lshl_b32 s10, s10, 1
	s_ashr_i32 s11, s10, 31
	s_lshl_b64 s[12:13], s[10:11], 10
	v_lshl_add_u64 v[68:69], v[20:21], 0, s[12:13]
	v_lshl_add_u64 v[82:83], v[22:23], 0, s[12:13]
	global_load_dwordx4 v[50:53], v[32:33], off
	s_waitcnt vmcnt(10)
	v_mfma_f32_32x32x16_f16 a[0:15], v[114:117], v[42:45], a[0:15]
	ds_read_b128 v[90:93], v27 offset:20480
	global_load_dwordx4 v[34:37], v[30:31], off
	v_mfma_f32_32x32x16_f16 a[0:15], v[114:117], v[38:41], a[0:15]
	ds_read_b128 v[94:97], v27 offset:33280
	global_load_dwordx4 v[30:33], v[66:67], off
	v_mfma_f32_32x32x16_f16 a[16:31], v[122:125], v[38:41], a[16:31]
	ds_read_b128 v[114:117], v27 offset:23040
	v_mfma_f32_32x32x16_f16 a[16:31], v[106:109], v[42:45], a[16:31]
	ds_read_b128 v[118:121], v27 offset:35840
	v_mfma_f32_32x32x16_f16 a[16:31], v[106:109], v[38:41], a[16:31]
	ds_read_b128 v[122:125], v27 offset:25600
	v_mfma_f32_32x32x16_f16 a[32:47], v[110:113], v[38:41], a[32:47]
	ds_read_b128 v[106:109], v27 offset:38400
	v_mfma_f32_32x32x16_f16 a[32:47], v[126:129], v[42:45], a[32:47]
	ds_read_b128 v[110:113], v27 offset:28160
	v_mfma_f32_32x32x16_f16 a[32:47], v[126:129], v[38:41], a[32:47]
	global_load_dwordx4 v[66:69], v[68:69], off
	s_nop 0
	global_load_dwordx4 v[82:85], v[82:83], off
	v_mfma_f32_32x32x16_f16 a[48:63], v[102:105], v[38:41], a[48:63]
	v_mfma_f32_32x32x16_f16 a[48:63], v[98:101], v[42:45], a[48:63]
	v_mfma_f32_32x32x16_f16 a[48:63], v[98:101], v[38:41], a[48:63]
	s_waitcnt vmcnt(9) lgkmcnt(7)
	v_mfma_f32_32x32x16_f16 a[0:15], v[86:89], v[70:73], a[0:15]
	ds_read_b128 v[98:101], v27 offset:30752
	s_or_b32 s10, s10, 1
	s_ashr_i32 s11, s10, 31
	s_lshl_b64 s[10:11], s[10:11], 10
	v_lshl_add_u64 v[38:39], v[20:21], 0, s[10:11]
	v_lshl_add_u64 v[42:43], v[22:23], 0, s[10:11]
	s_waitcnt vmcnt(8) lgkmcnt(7)
	v_mfma_f32_32x32x16_f16 a[0:15], v[90:93], v[78:81], a[0:15]
	ds_read_b128 v[86:89], v27 offset:20512
	v_mfma_f32_32x32x16_f16 a[0:15], v[90:93], v[70:73], a[0:15]
	ds_read_b128 v[126:129], v27 offset:33312
	s_waitcnt vmcnt(11)
	ds_write_b128 v28, v[62:65]
	s_waitcnt lgkmcnt(9)
	v_mfma_f32_32x32x16_f16 a[16:31], v[94:97], v[70:73], a[16:31]
	ds_read_b128 v[90:93], v27 offset:23072
	s_waitcnt lgkmcnt(9)
	v_mfma_f32_32x32x16_f16 a[16:31], v[114:117], v[78:81], a[16:31]
	ds_read_b128 v[130:133], v27 offset:35872
	s_waitcnt vmcnt(9)
	ds_write_b128 v28, v[74:77] offset:10240
	v_mfma_f32_32x32x16_f16 a[16:31], v[114:117], v[70:73], a[16:31]
	ds_read_b128 v[134:137], v27 offset:25632
	s_waitcnt lgkmcnt(11)
	v_mfma_f32_32x32x16_f16 a[32:47], v[118:121], v[70:73], a[32:47]
	ds_read_b128 v[138:141], v27 offset:38432
	ds_write_b128 v28, v[58:61] offset:5120
	s_waitcnt lgkmcnt(12)
	v_mfma_f32_32x32x16_f16 a[32:47], v[122:125], v[78:81], a[32:47]
	ds_read_b128 v[118:121], v27 offset:28192
	v_mfma_f32_32x32x16_f16 a[32:47], v[122:125], v[70:73], a[32:47]
	s_waitcnt vmcnt(10)
	ds_write_b128 v28, v[54:57] offset:15360
	global_load_dwordx4 v[38:41], v[38:39], off
	s_nop 0
	global_load_dwordx4 v[42:45], v[42:43], off
	s_waitcnt lgkmcnt(13)
	v_mfma_f32_32x32x16_f16 a[48:63], v[106:109], v[70:73], a[48:63]
	s_waitcnt lgkmcnt(12)
	v_mfma_f32_32x32x16_f16 a[48:63], v[110:113], v[78:81], a[48:63]
	v_mfma_f32_32x32x16_f16 a[48:63], v[110:113], v[70:73], a[48:63]
	s_min_i32 s10, s2, s8
	s_lshl_b32 s10, s10, 5
	s_ashr_i32 s11, s10, 31
	s_lshl_b64 s[10:11], s[10:11], 1
	v_lshl_add_u64 v[54:55], v[16:17], 0, s[10:11]
	s_waitcnt lgkmcnt(0)
	s_barrier
	global_load_dwordx4 v[62:65], v[54:55], off
	s_waitcnt vmcnt(10)
	v_mfma_f32_32x32x16_f16 a[0:15], v[98:101], v[0:3], a[0:15]
	ds_read_b128 v[114:117], v27 offset:10240
	v_lshl_add_u64 v[54:55], v[12:13], 0, s[10:11]
	v_lshl_add_u64 v[56:57], v[14:15], 0, s[10:11]
	v_lshl_add_u64 v[70:71], v[18:19], 0, s[10:11]
	s_lshl_b32 s10, s9, 1
	s_ashr_i32 s11, s10, 31
	s_lshl_b64 s[10:11], s[10:11], 10
	v_lshl_add_u64 v[72:73], v[20:21], 0, s[10:11]
	v_lshl_add_u64 v[78:79], v[22:23], 0, s[10:11]
	global_load_dwordx4 v[74:77], v[56:57], off
	s_waitcnt vmcnt(10)
	v_mfma_f32_32x32x16_f16 a[0:15], v[86:89], v[4:7], a[0:15]
	ds_read_b128 v[106:109], v27
	global_load_dwordx4 v[58:61], v[54:55], off
	v_mfma_f32_32x32x16_f16 a[0:15], v[86:89], v[0:3], a[0:15]
	ds_read_b128 v[110:113], v27 offset:12800
	global_load_dwordx4 v[54:57], v[70:71], off
	v_mfma_f32_32x32x16_f16 a[16:31], v[126:129], v[0:3], a[16:31]
	ds_read_b128 v[102:105], v27 offset:2560
	v_mfma_f32_32x32x16_f16 a[16:31], v[90:93], v[4:7], a[16:31]
	ds_read_b128 v[98:101], v27 offset:15360
	v_mfma_f32_32x32x16_f16 a[16:31], v[90:93], v[0:3], a[16:31]
	ds_read_b128 v[94:97], v27 offset:5120
	v_mfma_f32_32x32x16_f16 a[32:47], v[130:133], v[0:3], a[32:47]
	ds_read_b128 v[90:93], v27 offset:17920
	v_mfma_f32_32x32x16_f16 a[32:47], v[134:137], v[4:7], a[32:47]
	ds_read_b128 v[86:89], v27 offset:7680
	v_mfma_f32_32x32x16_f16 a[32:47], v[134:137], v[0:3], a[32:47]
	global_load_dwordx4 v[70:73], v[72:73], off
	s_nop 0
	global_load_dwordx4 v[78:81], v[78:79], off
	v_mfma_f32_32x32x16_f16 a[48:63], v[138:141], v[0:3], a[48:63]
	v_mfma_f32_32x32x16_f16 a[48:63], v[118:121], v[4:7], a[48:63]
	v_mfma_f32_32x32x16_f16 a[48:63], v[118:121], v[0:3], a[48:63]
	s_add_i32 s2, s2, 2
	s_add_i32 s3, s4, -2
	s_cmp_le_i32 s2, s3
	s_cbranch_scc1 .LBB16_6
.Ltail_LBB16:
	s_waitcnt lgkmcnt(0)
	s_waitcnt vmcnt(9)
	v_mfma_f32_32x32x16_f16 a[0:15], v[114:117], v[66:69], a[0:15]
	s_add_i32 s3, s2, -3
	s_min_i32 s3, s3, s8
	s_lshl_b32 s3, s3, 1
	ds_read_b128 v[118:121], v27 offset:10272
	s_or_b32 s10, s3, 1
	s_ashr_i32 s11, s10, 31
	s_lshl_b64 s[10:11], s[10:11], 10
	v_lshl_add_u64 v[0:1], v[20:21], 0, s[10:11]
	v_lshl_add_u64 v[4:5], v[22:23], 0, s[10:11]
	s_waitcnt vmcnt(7)
	v_mfma_f32_32x32x16_f16 a[0:15], v[106:109], v[82:85], a[0:15]
	ds_read_b128 v[114:117], v27 offset:32
	v_mfma_f32_32x32x16_f16 a[0:15], v[106:109], v[66:69], a[0:15]
	ds_read_b128 v[122:125], v27 offset:12832
	ds_write_b128 v28, v[46:49] offset:20480
	v_mfma_f32_32x32x16_f16 a[16:31], v[110:113], v[66:69], a[16:31]
	ds_read_b128 v[106:109], v27 offset:2592
	v_mfma_f32_32x32x16_f16 a[16:31], v[102:105], v[82:85], a[16:31]
	ds_read_b128 v[110:113], v27 offset:15392
	ds_write_b128 v28, v[50:53] offset:30720
	v_mfma_f32_32x32x16_f16 a[16:31], v[102:105], v[66:69], a[16:31]
	ds_read_b128 v[126:129], v27 offset:5152
	v_mfma_f32_32x32x16_f16 a[32:47], v[98:101], v[66:69], a[32:47]
	ds_read_b128 v[102:105], v27 offset:17952
	ds_write_b128 v28, v[34:37] offset:25600
	v_mfma_f32_32x32x16_f16 a[32:47], v[94:97], v[82:85], a[32:47]
	ds_read_b128 v[98:101], v27 offset:7712
	v_mfma_f32_32x32x16_f16 a[32:47], v[94:97], v[66:69], a[32:47]
	ds_write_b128 v28, v[30:33] offset:35840
	global_load_dwordx4 v[0:3], v[0:1], off
	s_nop 0
	global_load_dwordx4 v[4:7], v[4:5], off
	v_mfma_f32_32x32x16_f16 a[48:63], v[90:93], v[66:69], a[48:63]
	v_mfma_f32_32x32x16_f16 a[48:63], v[86:89], v[82:85], a[48:63]
	v_mfma_f32_32x32x16_f16 a[48:63], v[86:89], v[66:69], a[48:63]
	s_add_i32 s3, s2, -1
	s_min_i32 s9, s3, s8
	s_lshl_b32 s10, s9, 5
	s_ashr_i32 s11, s10, 31
	s_lshl_b64 s[10:11], s[10:11], 1
	v_lshl_add_u64 v[30:31], v[16:17], 0, s[10:11]
	s_waitcnt lgkmcnt(0)
	s_barrier
	global_load_dwordx4 v[46:49], v[30:31], off
	v_mfma_f32_32x32x16_f16 a[0:15], v[118:121], v[38:41], a[0:15]
	s_add_i32 s3, s2, -2
	v_lshl_add_u64 v[30:31], v[12:13], 0, s[10:11]
	v_lshl_add_u64 v[32:33], v[14:15], 0, s[10:11]
	v_lshl_add_u64 v[66:67], v[18:19], 0, s[10:11]
	s_min_i32 s10, s3, s8
	ds_read_b128 v[86:89], v27 offset:30720
	s_lshl_b32 s10, s10, 1
	s_ashr_i32 s11, s10, 31
	s_lshl_b64 s[12:13], s[10:11], 10
	v_lshl_add_u64 v[68:69], v[20:21], 0, s[12:13]
	v_lshl_add_u64 v[82:83], v[22:23], 0, s[12:13]
	global_load_dwordx4 v[50:53], v[32:33], off
	s_waitcnt vmcnt(10)
	v_mfma_f32_32x32x16_f16 a[0:15], v[114:117], v[42:45], a[0:15]
	ds_read_b128 v[90:93], v27 offset:20480
	global_load_dwordx4 v[34:37], v[30:31], off
	v_mfma_f32_32x32x16_f16 a[0:15], v[114:117], v[38:41], a[0:15]
	ds_read_b128 v[94:97], v27 offset:33280
	global_load_dwordx4 v[30:33], v[66:67], off
	v_mfma_f32_32x32x16_f16 a[16:31], v[122:125], v[38:41], a[16:31]
	ds_read_b128 v[114:117], v27 offset:23040
	v_mfma_f32_32x32x16_f16 a[16:31], v[106:109], v[42:45], a[16:31]
	ds_read_b128 v[118:121], v27 offset:35840
	v_mfma_f32_32x32x16_f16 a[16:31], v[106:109], v[38:41], a[16:31]
	ds_read_b128 v[122:125], v27 offset:25600
	v_mfma_f32_32x32x16_f16 a[32:47], v[110:113], v[38:41], a[32:47]
	ds_read_b128 v[106:109], v27 offset:38400
	v_mfma_f32_32x32x16_f16 a[32:47], v[126:129], v[42:45], a[32:47]
	ds_read_b128 v[110:113], v27 offset:28160
	v_mfma_f32_32x32x16_f16 a[32:47], v[126:129], v[38:41], a[32:47]
	global_load_dwordx4 v[66:69], v[68:69], off
	s_nop 0
	global_load_dwordx4 v[82:85], v[82:83], off
	v_mfma_f32_32x32x16_f16 a[48:63], v[102:105], v[38:41], a[48:63]
	v_mfma_f32_32x32x16_f16 a[48:63], v[98:101], v[42:45], a[48:63]
	v_mfma_f32_32x32x16_f16 a[48:63], v[98:101], v[38:41], a[48:63]
	s_waitcnt lgkmcnt(7)
	s_waitcnt vmcnt(9)
	v_mfma_f32_32x32x16_f16 a[0:15], v[86:89], v[70:73], a[0:15]
	ds_read_b128 v[98:101], v27 offset:30752
	s_or_b32 s10, s10, 1
	s_ashr_i32 s11, s10, 31
	s_lshl_b64 s[10:11], s[10:11], 10
	v_lshl_add_u64 v[38:39], v[20:21], 0, s[10:11]
	v_lshl_add_u64 v[42:43], v[22:23], 0, s[10:11]
	s_waitcnt lgkmcnt(7)
	s_waitcnt vmcnt(8)
	v_mfma_f32_32x32x16_f16 a[0:15], v[90:93], v[78:81], a[0:15]
	ds_read_b128 v[86:89], v27 offset:20512
	v_mfma_f32_32x32x16_f16 a[0:15], v[90:93], v[70:73], a[0:15]
	ds_read_b128 v[126:129], v27 offset:33312
	s_waitcnt vmcnt(11)
	ds_write_b128 v28, v[62:65]
	s_waitcnt lgkmcnt(9)
	v_mfma_f32_32x32x16_f16 a[16:31], v[94:97], v[70:73], a[16:31]
	ds_read_b128 v[90:93], v27 offset:23072
	s_waitcnt lgkmcnt(9)
	v_mfma_f32_32x32x16_f16 a[16:31], v[114:117], v[78:81], a[16:31]
	ds_read_b128 v[130:133], v27 offset:35872
	s_waitcnt vmcnt(9)
	ds_write_b128 v28, v[74:77] offset:10240
	v_mfma_f32_32x32x16_f16 a[16:31], v[114:117], v[70:73], a[16:31]
	ds_read_b128 v[134:137], v27 offset:25632
	s_waitcnt lgkmcnt(11)
	v_mfma_f32_32x32x16_f16 a[32:47], v[118:121], v[70:73], a[32:47]
	ds_read_b128 v[138:141], v27 offset:38432
	ds_write_b128 v28, v[58:61] offset:5120
	s_waitcnt lgkmcnt(12)
	v_mfma_f32_32x32x16_f16 a[32:47], v[122:125], v[78:81], a[32:47]
	ds_read_b128 v[118:121], v27 offset:28192
	v_mfma_f32_32x32x16_f16 a[32:47], v[122:125], v[70:73], a[32:47]
	s_waitcnt vmcnt(8)
	ds_write_b128 v28, v[54:57] offset:15360
	global_load_dwordx4 v[38:41], v[38:39], off
	s_nop 0
	global_load_dwordx4 v[42:45], v[42:43], off
	s_waitcnt lgkmcnt(13)
	v_mfma_f32_32x32x16_f16 a[48:63], v[106:109], v[70:73], a[48:63]
	s_waitcnt lgkmcnt(12)
	v_mfma_f32_32x32x16_f16 a[48:63], v[110:113], v[78:81], a[48:63]
	v_mfma_f32_32x32x16_f16 a[48:63], v[110:113], v[70:73], a[48:63]
	s_min_i32 s10, s2, s8
	s_lshl_b32 s10, s10, 5
	s_ashr_i32 s11, s10, 31
	s_lshl_b64 s[10:11], s[10:11], 1
	v_lshl_add_u64 v[54:55], v[16:17], 0, s[10:11]
	s_waitcnt lgkmcnt(0)
	s_barrier
	s_waitcnt vmcnt(9)
	v_mfma_f32_32x32x16_f16 a[0:15], v[98:101], v[0:3], a[0:15]
	ds_read_b128 v[114:117], v27 offset:10240
	v_lshl_add_u64 v[54:55], v[12:13], 0, s[10:11]
	v_lshl_add_u64 v[56:57], v[14:15], 0, s[10:11]
	v_lshl_add_u64 v[70:71], v[18:19], 0, s[10:11]
	s_lshl_b32 s10, s9, 1
	s_ashr_i32 s11, s10, 31
	s_lshl_b64 s[10:11], s[10:11], 10
	v_lshl_add_u64 v[72:73], v[20:21], 0, s[10:11]
	v_lshl_add_u64 v[78:79], v[22:23], 0, s[10:11]
	s_waitcnt vmcnt(8)
	v_mfma_f32_32x32x16_f16 a[0:15], v[86:89], v[4:7], a[0:15]
	ds_read_b128 v[106:109], v27
	v_mfma_f32_32x32x16_f16 a[0:15], v[86:89], v[0:3], a[0:15]
	ds_read_b128 v[110:113], v27 offset:12800
	v_mfma_f32_32x32x16_f16 a[16:31], v[126:129], v[0:3], a[16:31]
	ds_read_b128 v[102:105], v27 offset:2560
	v_mfma_f32_32x32x16_f16 a[16:31], v[90:93], v[4:7], a[16:31]
	ds_read_b128 v[98:101], v27 offset:15360
	v_mfma_f32_32x32x16_f16 a[16:31], v[90:93], v[0:3], a[16:31]
	ds_read_b128 v[94:97], v27 offset:5120
	v_mfma_f32_32x32x16_f16 a[32:47], v[130:133], v[0:3], a[32:47]
	ds_read_b128 v[90:93], v27 offset:17920
	v_mfma_f32_32x32x16_f16 a[32:47], v[134:137], v[4:7], a[32:47]
	ds_read_b128 v[86:89], v27 offset:7680
	v_mfma_f32_32x32x16_f16 a[32:47], v[134:137], v[0:3], a[32:47]
	global_load_dwordx4 v[70:73], v[72:73], off
	s_nop 0
	global_load_dwordx4 v[78:81], v[78:79], off
	v_mfma_f32_32x32x16_f16 a[48:63], v[138:141], v[0:3], a[48:63]
	v_mfma_f32_32x32x16_f16 a[48:63], v[118:121], v[4:7], a[48:63]
	v_mfma_f32_32x32x16_f16 a[48:63], v[118:121], v[0:3], a[48:63]
	s_add_i32 s2, s2, 2
	s_waitcnt lgkmcnt(0)
	s_waitcnt vmcnt(5)
	v_mfma_f32_32x32x16_f16 a[0:15], v[114:117], v[66:69], a[0:15]
	s_add_i32 s3, s2, -3
	s_min_i32 s3, s3, s8
	s_lshl_b32 s3, s3, 1
	ds_read_b128 v[118:121], v27 offset:10272
	s_or_b32 s10, s3, 1
	s_ashr_i32 s11, s10, 31
	s_lshl_b64 s[10:11], s[10:11], 10
	v_lshl_add_u64 v[0:1], v[20:21], 0, s[10:11]
	v_lshl_add_u64 v[4:5], v[22:23], 0, s[10:11]
	s_waitcnt vmcnt(4)
	v_mfma_f32_32x32x16_f16 a[0:15], v[106:109], v[82:85], a[0:15]
	ds_read_b128 v[114:117], v27 offset:32
	v_mfma_f32_32x32x16_f16 a[0:15], v[106:109], v[66:69], a[0:15]
	ds_read_b128 v[122:125], v27 offset:12832
	ds_write_b128 v28, v[46:49] offset:20480
	v_mfma_f32_32x32x16_f16 a[16:31], v[110:113], v[66:69], a[16:31]
	ds_read_b128 v[106:109], v27 offset:2592
	v_mfma_f32_32x32x16_f16 a[16:31], v[102:105], v[82:85], a[16:31]
	ds_read_b128 v[110:113], v27 offset:15392
	ds_write_b128 v28, v[50:53] offset:30720
	v_mfma_f32_32x32x16_f16 a[16:31], v[102:105], v[66:69], a[16:31]
	ds_read_b128 v[126:129], v27 offset:5152
	v_mfma_f32_32x32x16_f16 a[32:47], v[98:101], v[66:69], a[32:47]
	ds_read_b128 v[102:105], v27 offset:17952
	ds_write_b128 v28, v[34:37] offset:25600
	v_mfma_f32_32x32x16_f16 a[32:47], v[94:97], v[82:85], a[32:47]
	ds_read_b128 v[98:101], v27 offset:7712
	v_mfma_f32_32x32x16_f16 a[32:47], v[94:97], v[66:69], a[32:47]
	ds_write_b128 v28, v[30:33] offset:35840
	global_load_dwordx4 v[0:3], v[0:1], off
	s_nop 0
	global_load_dwordx4 v[4:7], v[4:5], off
	v_mfma_f32_32x32x16_f16 a[48:63], v[90:93], v[66:69], a[48:63]
	v_mfma_f32_32x32x16_f16 a[48:63], v[86:89], v[82:85], a[48:63]
	v_mfma_f32_32x32x16_f16 a[48:63], v[86:89], v[66:69], a[48:63]
	s_add_i32 s3, s2, -1
	s_min_i32 s9, s3, s8
	s_lshl_b32 s10, s9, 5
	s_ashr_i32 s11, s10, 31
	s_lshl_b64 s[10:11], s[10:11], 1
	v_lshl_add_u64 v[30:31], v[16:17], 0, s[10:11]
	s_waitcnt lgkmcnt(0)
	s_barrier
	s_waitcnt vmcnt(5)
	v_mfma_f32_32x32x16_f16 a[0:15], v[118:121], v[38:41], a[0:15]
	s_add_i32 s3, s2, -2
	v_lshl_add_u64 v[30:31], v[12:13], 0, s[10:11]
	v_lshl_add_u64 v[32:33], v[14:15], 0, s[10:11]
	v_lshl_add_u64 v[66:67], v[18:19], 0, s[10:11]
	s_min_i32 s10, s3, s8
	ds_read_b128 v[86:89], v27 offset:30720
	s_lshl_b32 s10, s10, 1
	s_ashr_i32 s11, s10, 31
	s_lshl_b64 s[12:13], s[10:11], 10
	v_lshl_add_u64 v[68:69], v[20:21], 0, s[12:13]
	v_lshl_add_u64 v[82:83], v[22:23], 0, s[12:13]
	s_waitcnt vmcnt(4)
	v_mfma_f32_32x32x16_f16 a[0:15], v[114:117], v[42:45], a[0:15]
	ds_read_b128 v[90:93], v27 offset:20480
	v_mfma_f32_32x32x16_f16 a[0:15], v[114:117], v[38:41], a[0:15]
	ds_read_b128 v[94:97], v27 offset:33280
	v_mfma_f32_32x32x16_f16 a[16:31], v[122:125], v[38:41], a[16:31]
	ds_read_b128 v[114:117], v27 offset:23040
	v_mfma_f32_32x32x16_f16 a[16:31], v[106:109], v[42:45], a[16:31]
	ds_read_b128 v[118:121], v27 offset:35840
	v_mfma_f32_32x32x16_f16 a[16:31], v[106:109], v[38:41], a[16:31]
	ds_read_b128 v[122:125], v27 offset:25600
	v_mfma_f32_32x32x16_f16 a[32:47], v[110:113], v[38:41], a[32:47]
	ds_read_b128 v[106:109], v27 offset:38400
	v_mfma_f32_32x32x16_f16 a[32:47], v[126:129], v[42:45], a[32:47]
	ds_read_b128 v[110:113], v27 offset:28160
	v_mfma_f32_32x32x16_f16 a[32:47], v[126:129], v[38:41], a[32:47]
	v_mfma_f32_32x32x16_f16 a[48:63], v[102:105], v[38:41], a[48:63]
	v_mfma_f32_32x32x16_f16 a[48:63], v[98:101], v[42:45], a[48:63]
	v_mfma_f32_32x32x16_f16 a[48:63], v[98:101], v[38:41], a[48:63]
	s_waitcnt lgkmcnt(7)
	s_waitcnt vmcnt(3)
	v_mfma_f32_32x32x16_f16 a[0:15], v[86:89], v[70:73], a[0:15]
	ds_read_b128 v[98:101], v27 offset:30752
	s_or_b32 s10, s10, 1
	s_ashr_i32 s11, s10, 31
	s_lshl_b64 s[10:11], s[10:11], 10
	v_lshl_add_u64 v[38:39], v[20:21], 0, s[10:11]
	v_lshl_add_u64 v[42:43], v[22:23], 0, s[10:11]
	s_waitcnt lgkmcnt(7)
	s_waitcnt vmcnt(2)
	v_mfma_f32_32x32x16_f16 a[0:15], v[90:93], v[78:81], a[0:15]
	ds_read_b128 v[86:89], v27 offset:20512
	v_mfma_f32_32x32x16_f16 a[0:15], v[90:93], v[70:73], a[0:15]
	ds_read_b128 v[126:129], v27 offset:33312
	ds_write_b128 v28, v[62:65]
	s_waitcnt lgkmcnt(9)
	v_mfma_f32_32x32x16_f16 a[16:31], v[94:97], v[70:73], a[16:31]
	ds_read_b128 v[90:93], v27 offset:23072
	s_waitcnt lgkmcnt(9)
	v_mfma_f32_32x32x16_f16 a[16:31], v[114:117], v[78:81], a[16:31]
	ds_read_b128 v[130:133], v27 offset:35872
	ds_write_b128 v28, v[74:77] offset:10240
	v_mfma_f32_32x32x16_f16 a[16:31], v[114:117], v[70:73], a[16:31]
	ds_read_b128 v[134:137], v27 offset:25632
	s_waitcnt lgkmcnt(11)
	v_mfma_f32_32x32x16_f16 a[32:47], v[118:121], v[70:73], a[32:47]
	ds_read_b128 v[138:141], v27 offset:38432
	ds_write_b128 v28, v[58:61] offset:5120
	s_waitcnt lgkmcnt(12)
	v_mfma_f32_32x32x16_f16 a[32:47], v[122:125], v[78:81], a[32:47]
	ds_read_b128 v[118:121], v27 offset:28192
	v_mfma_f32_32x32x16_f16 a[32:47], v[122:125], v[70:73], a[32:47]
	ds_write_b128 v28, v[54:57] offset:15360
	s_waitcnt lgkmcnt(13)
	v_mfma_f32_32x32x16_f16 a[48:63], v[106:109], v[70:73], a[48:63]
	s_waitcnt lgkmcnt(12)
	v_mfma_f32_32x32x16_f16 a[48:63], v[110:113], v[78:81], a[48:63]
	v_mfma_f32_32x32x16_f16 a[48:63], v[110:113], v[70:73], a[48:63]
	s_min_i32 s10, s2, s8
	s_lshl_b32 s10, s10, 5
	s_ashr_i32 s11, s10, 31
	s_lshl_b64 s[10:11], s[10:11], 1
	v_lshl_add_u64 v[54:55], v[16:17], 0, s[10:11]
	s_waitcnt lgkmcnt(0)
	s_barrier
	s_waitcnt vmcnt(1)
	v_mfma_f32_32x32x16_f16 a[0:15], v[98:101], v[0:3], a[0:15]
	ds_read_b128 v[114:117], v27 offset:10240
	v_lshl_add_u64 v[54:55], v[12:13], 0, s[10:11]
	v_lshl_add_u64 v[56:57], v[14:15], 0, s[10:11]
	v_lshl_add_u64 v[70:71], v[18:19], 0, s[10:11]
	s_lshl_b32 s10, s9, 1
	s_ashr_i32 s11, s10, 31
	s_lshl_b64 s[10:11], s[10:11], 10
	v_lshl_add_u64 v[72:73], v[20:21], 0, s[10:11]
	v_lshl_add_u64 v[78:79], v[22:23], 0, s[10:11]
	s_waitcnt vmcnt(0)
	v_mfma_f32_32x32x16_f16 a[0:15], v[86:89], v[4:7], a[0:15]
	ds_read_b128 v[106:109], v27
	v_mfma_f32_32x32x16_f16 a[0:15], v[86:89], v[0:3], a[0:15]
	ds_read_b128 v[110:113], v27 offset:12800
	v_mfma_f32_32x32x16_f16 a[16:31], v[126:129], v[0:3], a[16:31]
	ds_read_b128 v[102:105], v27 offset:2560
	v_mfma_f32_32x32x16_f16 a[16:31], v[90:93], v[4:7], a[16:31]
	ds_read_b128 v[98:101], v27 offset:15360
	v_mfma_f32_32x32x16_f16 a[16:31], v[90:93], v[0:3], a[16:31]
	ds_read_b128 v[94:97], v27 offset:5120
	v_mfma_f32_32x32x16_f16 a[32:47], v[130:133], v[0:3], a[32:47]
	ds_read_b128 v[90:93], v27 offset:17920
	v_mfma_f32_32x32x16_f16 a[32:47], v[134:137], v[4:7], a[32:47]
	ds_read_b128 v[86:89], v27 offset:7680
	v_mfma_f32_32x32x16_f16 a[32:47], v[134:137], v[0:3], a[32:47]
	v_mfma_f32_32x32x16_f16 a[48:63], v[138:141], v[0:3], a[48:63]
	v_mfma_f32_32x32x16_f16 a[48:63], v[118:121], v[4:7], a[48:63]
	v_mfma_f32_32x32x16_f16 a[48:63], v[118:121], v[0:3], a[48:63]
.LBB16_7:
	s_waitcnt vmcnt(0)
	s_load_dwordx4 s[8:11], s[0:1], 0x50
	s_waitcnt vmcnt(4)
	v_mul_u32_u24_e32 v76, 0x2800, v11
	s_load_dword s24, s[0:1], 0x6c
	s_load_dwordx2 s[0:1], s[0:1], 0x40
	v_ashrrev_i32_e32 v11, 31, v10
	v_mov_b32_e32 v0, s6
	v_lshrrev_b32_e32 v4, 2, v25
	v_accvgpr_read_b32 v75, a0
	s_waitcnt lgkmcnt(0)
	s_lshl_b32 s24, s24, 7
	s_mov_b32 s0, 32
	s_mov_b32 s1, 0
	v_mul_lo_u32 v10, v10, s24
	v_mov_b32_e32 v11, 0
	s_mul_i32 s2, s1, s6
	s_mul_i32 s3, s0, s7
	s_add_i32 s4, s3, s2
	v_mad_u64_u32 v[0:1], s[2:3], s0, v0, v[10:11]
	v_or_b32_e32 v0, v0, v8
	v_lshl_or_b32 v77, v8, 1, v76
	v_mul_u32_u24_e32 v8, 40, v4
	s_waitcnt vmcnt(0)
	v_lshl_add_u32 v78, v8, 1, v77
	v_fma_f32 v8, s5, v75, v9
	v_max_f32_e32 v8, 0, v8
	s_mov_b32 s2, 0x43800000
	v_mul_u32_u24_e32 v11, 0xa0, v26
	v_fma_mixlo_f16 v10, v8, s2, 0
	v_or_b32_e32 v11, v11, v24
	v_accvgpr_read_b32 v74, a1
	v_fma_mixlo_f16 v8, v8, s2, -v10 op_sel_hi:[0,0,1]
	v_lshl_or_b32 v26, v11, 1, v76
	s_barrier
	ds_write_b16 v26, v10
	ds_write_b16 v26, v8 offset:5120
	v_fma_f32 v8, s5, v74, v9
	v_max_f32_e32 v8, 0, v8
	v_fma_mixlo_f16 v10, v8, s2, 0
	v_accvgpr_read_b32 v73, a2
	v_fma_mixlo_f16 v8, v8, s2, -v10 op_sel_hi:[0,0,1]
	ds_write_b16 v26, v10 offset:80
	ds_write_b16 v26, v8 offset:5200
	v_fma_f32 v8, s5, v73, v9
	v_max_f32_e32 v8, 0, v8
	v_fma_mixlo_f16 v10, v8, s2, 0
	v_accvgpr_read_b32 v72, a3
	v_fma_mixlo_f16 v8, v8, s2, -v10 op_sel_hi:[0,0,1]
	ds_write_b16 v26, v10 offset:160
	ds_write_b16 v26, v8 offset:5280
	v_fma_f32 v8, s5, v72, v9
	v_max_f32_e32 v8, 0, v8
	v_fma_mixlo_f16 v10, v8, s2, 0
	v_accvgpr_read_b32 v71, a4
	v_fma_mixlo_f16 v8, v8, s2, -v10 op_sel_hi:[0,0,1]
	ds_write_b16 v26, v10 offset:240
	ds_write_b16 v26, v8 offset:5360
	v_fma_f32 v8, s5, v71, v9
	v_max_f32_e32 v8, 0, v8
	v_fma_mixlo_f16 v10, v8, s2, 0
	v_accvgpr_read_b32 v70, a5
	v_fma_mixlo_f16 v8, v8, s2, -v10 op_sel_hi:[0,0,1]
	ds_write_b16 v26, v10 offset:640
	ds_write_b16 v26, v8 offset:5760
	v_fma_f32 v8, s5, v70, v9
	v_max_f32_e32 v8, 0, v8
	v_fma_mixlo_f16 v10, v8, s2, 0
	v_accvgpr_read_b32 v69, a6
	v_fma_mixlo_f16 v8, v8, s2, -v10 op_sel_hi:[0,0,1]
	ds_write_b16 v26, v10 offset:720
	ds_write_b16 v26, v8 offset:5840
	v_fma_f32 v8, s5, v69, v9
	v_max_f32_e32 v8, 0, v8
	v_fma_mixlo_f16 v10, v8, s2, 0
	v_accvgpr_read_b32 v68, a7
	v_fma_mixlo_f16 v8, v8, s2, -v10 op_sel_hi:[0,0,1]
	ds_write_b16 v26, v10 offset:800
	ds_write_b16 v26, v8 offset:5920
	v_fma_f32 v8, s5, v68, v9
	v_max_f32_e32 v8, 0, v8
	v_fma_mixlo_f16 v10, v8, s2, 0
	v_accvgpr_read_b32 v67, a8
	v_fma_mixlo_f16 v8, v8, s2, -v10 op_sel_hi:[0,0,1]
	ds_write_b16 v26, v10 offset:880
	ds_write_b16 v26, v8 offset:6000
	v_fma_f32 v8, s5, v67, v9
	v_max_f32_e32 v8, 0, v8
	v_fma_mixlo_f16 v10, v8, s2, 0
	v_accvgpr_read_b32 v66, a9
	v_fma_mixlo_f16 v8, v8, s2, -v10 op_sel_hi:[0,0,1]
	ds_write_b16 v26, v10 offset:1280
	ds_write_b16 v26, v8 offset:6400
	v_fma_f32 v8, s5, v66, v9
	v_max_f32_e32 v8, 0, v8
	v_fma_mixlo_f16 v10, v8, s2, 0
	v_accvgpr_read_b32 v65, a10
	v_fma_mixlo_f16 v8, v8, s2, -v10 op_sel_hi:[0,0,1]
	ds_write_b16 v26, v10 offset:1360
	ds_write_b16 v26, v8 offset:6480
	v_fma_f32 v8, s5, v65, v9
	v_max_f32_e32 v8, 0, v8
	v_fma_mixlo_f16 v10, v8, s2, 0
	v_accvgpr_read_b32 v64, a11
	v_fma_mixlo_f16 v8, v8, s2, -v10 op_sel_hi:[0,0,1]
	ds_write_b16 v26, v10 offset:1440
	ds_write_b16 v26, v8 offset:6560
	v_fma_f32 v8, s5, v64, v9
	v_max_f32_e32 v8, 0, v8
	v_fma_mixlo_f16 v10, v8, s2, 0
	v_accvgpr_read_b32 v63, a12
	v_fma_mixlo_f16 v8, v8, s2, -v10 op_sel_hi:[0,0,1]
	ds_write_b16 v26, v10 offset:1520
	ds_write_b16 v26, v8 offset:6640
	v_fma_f32 v8, s5, v63, v9
	v_max_f32_e32 v8, 0, v8
	v_fma_mixlo_f16 v10, v8, s2, 0
	v_accvgpr_read_b32 v62, a13
	v_fma_mixlo_f16 v8, v8, s2, -v10 op_sel_hi:[0,0,1]
	ds_write_b16 v26, v10 offset:1920
	ds_write_b16 v26, v8 offset:7040
	v_fma_f32 v8, s5, v62, v9
	v_max_f32_e32 v8, 0, v8
	v_fma_mixlo_f16 v10, v8, s2, 0
	v_accvgpr_read_b32 v61, a14
	v_fma_mixlo_f16 v8, v8, s2, -v10 op_sel_hi:[0,0,1]
	ds_write_b16 v26, v10 offset:2000
	ds_write_b16 v26, v8 offset:7120
	v_fma_f32 v8, s5, v61, v9
	v_max_f32_e32 v8, 0, v8
	v_fma_mixlo_f16 v10, v8, s2, 0
	v_accvgpr_read_b32 v60, a15
	v_fma_mixlo_f16 v8, v8, s2, -v10 op_sel_hi:[0,0,1]
	ds_write_b16 v26, v10 offset:2080
	ds_write_b16 v26, v8 offset:7200
	v_fma_f32 v8, s5, v60, v9
	v_max_f32_e32 v8, 0, v8
	v_fma_mixlo_f16 v10, v8, s2, 0
	v_accvgpr_read_b32 v59, a16
	v_fma_mixlo_f16 v8, v8, s2, -v10 op_sel_hi:[0,0,1]
	ds_write_b16 v26, v10 offset:2160
	ds_write_b16 v26, v8 offset:7280
	v_fma_f32 v8, s5, v59, v9
	v_max_f32_e32 v8, 0, v8
	v_fma_mixlo_f16 v10, v8, s2, 0
	v_accvgpr_read_b32 v58, a17
	v_fma_mixlo_f16 v8, v8, s2, -v10 op_sel_hi:[0,0,1]
	ds_write_b16 v26, v10 offset:2560
	ds_write_b16 v26, v8 offset:7680
	v_fma_f32 v8, s5, v58, v9
	v_max_f32_e32 v8, 0, v8
	v_fma_mixlo_f16 v10, v8, s2, 0
	v_accvgpr_read_b32 v57, a18
	v_fma_mixlo_f16 v8, v8, s2, -v10 op_sel_hi:[0,0,1]
	ds_write_b16 v26, v10 offset:2640
	ds_write_b16 v26, v8 offset:7760
	v_fma_f32 v8, s5, v57, v9
	v_max_f32_e32 v8, 0, v8
	v_fma_mixlo_f16 v10, v8, s2, 0
	v_accvgpr_read_b32 v56, a19
	v_fma_mixlo_f16 v8, v8, s2, -v10 op_sel_hi:[0,0,1]
	ds_write_b16 v26, v10 offset:2720
	ds_write_b16 v26, v8 offset:7840
	v_fma_f32 v8, s5, v56, v9
	v_max_f32_e32 v8, 0, v8
	v_fma_mixlo_f16 v10, v8, s2, 0
	v_accvgpr_read_b32 v55, a20
	v_fma_mixlo_f16 v8, v8, s2, -v10 op_sel_hi:[0,0,1]
	ds_write_b16 v26, v10 offset:2800
	ds_write_b16 v26, v8 offset:7920
	v_fma_f32 v8, s5, v55, v9
	v_max_f32_e32 v8, 0, v8
	v_fma_mixlo_f16 v10, v8, s2, 0
	v_accvgpr_read_b32 v54, a21
	v_fma_mixlo_f16 v8, v8, s2, -v10 op_sel_hi:[0,0,1]
	ds_write_b16 v26, v10 offset:3200
	ds_write_b16 v26, v8 offset:8320
	v_fma_f32 v8, s5, v54, v9
	v_max_f32_e32 v8, 0, v8
	v_fma_mixlo_f16 v10, v8, s2, 0
	v_accvgpr_read_b32 v53, a22
	v_fma_mixlo_f16 v8, v8, s2, -v10 op_sel_hi:[0,0,1]
	ds_write_b16 v26, v10 offset:3280
	ds_write_b16 v26, v8 offset:8400
	v_fma_f32 v8, s5, v53, v9
	v_max_f32_e32 v8, 0, v8
	v_fma_mixlo_f16 v10, v8, s2, 0
	v_accvgpr_read_b32 v52, a23
	v_fma_mixlo_f16 v8, v8, s2, -v10 op_sel_hi:[0,0,1]
	ds_write_b16 v26, v10 offset:3360
	ds_write_b16 v26, v8 offset:8480
	v_fma_f32 v8, s5, v52, v9
	v_max_f32_e32 v8, 0, v8
	v_fma_mixlo_f16 v10, v8, s2, 0
	v_accvgpr_read_b32 v51, a24
	v_fma_mixlo_f16 v8, v8, s2, -v10 op_sel_hi:[0,0,1]
	ds_write_b16 v26, v10 offset:3440
	ds_write_b16 v26, v8 offset:8560
	v_fma_f32 v8, s5, v51, v9
	v_max_f32_e32 v8, 0, v8
	v_fma_mixlo_f16 v10, v8, s2, 0
	v_accvgpr_read_b32 v50, a25
	v_fma_mixlo_f16 v8, v8, s2, -v10 op_sel_hi:[0,0,1]
	ds_write_b16 v26, v10 offset:3840
	ds_write_b16 v26, v8 offset:8960
	v_fma_f32 v8, s5, v50, v9
	v_max_f32_e32 v8, 0, v8
	v_fma_mixlo_f16 v10, v8, s2, 0
	v_accvgpr_read_b32 v49, a26
	v_fma_mixlo_f16 v8, v8, s2, -v10 op_sel_hi:[0,0,1]
	ds_write_b16 v26, v10 offset:3920
	ds_write_b16 v26, v8 offset:9040
	v_fma_f32 v8, s5, v49, v9
	v_max_f32_e32 v8, 0, v8
	v_fma_mixlo_f16 v10, v8, s2, 0
	v_accvgpr_read_b32 v48, a27
	v_fma_mixlo_f16 v8, v8, s2, -v10 op_sel_hi:[0,0,1]
	ds_write_b16 v26, v10 offset:4000
	ds_write_b16 v26, v8 offset:9120
	v_fma_f32 v8, s5, v48, v9
	v_max_f32_e32 v8, 0, v8
	v_fma_mixlo_f16 v10, v8, s2, 0
	v_accvgpr_read_b32 v47, a28
	v_fma_mixlo_f16 v8, v8, s2, -v10 op_sel_hi:[0,0,1]
	ds_write_b16 v26, v10 offset:4080
	ds_write_b16 v26, v8 offset:9200
	v_fma_f32 v8, s5, v47, v9
	v_max_f32_e32 v8, 0, v8
	v_fma_mixlo_f16 v10, v8, s2, 0
	v_accvgpr_read_b32 v46, a29
	v_fma_mixlo_f16 v8, v8, s2, -v10 op_sel_hi:[0,0,1]
	ds_write_b16 v26, v10 offset:4480
	ds_write_b16 v26, v8 offset:9600
	v_fma_f32 v8, s5, v46, v9
	v_max_f32_e32 v8, 0, v8
	v_fma_mixlo_f16 v10, v8, s2, 0
	v_accvgpr_read_b32 v45, a30
	v_fma_mixlo_f16 v8, v8, s2, -v10 op_sel_hi:[0,0,1]
	ds_write_b16 v26, v10 offset:4560
	ds_write_b16 v26, v8 offset:9680
	v_fma_f32 v8, s5, v45, v9
	v_max_f32_e32 v8, 0, v8
	v_fma_mixlo_f16 v10, v8, s2, 0
	v_accvgpr_read_b32 v44, a31
	v_fma_mixlo_f16 v8, v8, s2, -v10 op_sel_hi:[0,0,1]
	ds_write_b16 v26, v10 offset:4640
	ds_write_b16 v26, v8 offset:9760
	v_fma_f32 v8, s5, v44, v9
	v_max_f32_e32 v8, 0, v8
	v_fma_mixlo_f16 v10, v8, s2, 0
	v_fma_mixlo_f16 v8, v8, s2, -v10 op_sel_hi:[0,0,1]
	ds_write_b16 v26, v10 offset:4720
	ds_write_b16 v26, v8 offset:9840
	v_mad_u64_u32 v[10:11], s[6:7], s0, v4, 0
	v_mov_b32_e32 v8, v11
	v_add_u32_e32 v1, s4, v1
	ds_read_b128 v[44:47], v78
	ds_read_b128 v[48:51], v78 offset:5120
	v_mad_u64_u32 v[24:25], s[6:7], s1, v4, v[8:9]
	v_lshlrev_b64 v[0:1], 1, v[0:1]
	v_mov_b32_e32 v11, v24
	v_lshl_add_u64 v[2:3], s[8:9], 0, v[0:1]
	v_lshlrev_b64 v[10:11], 1, v[10:11]
	v_lshl_add_u64 v[0:1], s[10:11], 0, v[0:1]
	v_lshl_add_u64 v[24:25], v[2:3], 0, v[10:11]
	s_waitcnt lgkmcnt(1)
	global_store_dwordx4 v[24:25], v[44:47], off sc1
	v_lshl_add_u64 v[10:11], v[0:1], 0, v[10:11]
	v_or_b32_e32 v24, 16, v4
	s_waitcnt lgkmcnt(0)
	global_store_dwordx4 v[10:11], v[48:51], off sc1
	v_mul_u32_u24_e32 v8, 40, v24
	v_mad_u64_u32 v[10:11], s[6:7], s0, v24, 0
	v_lshl_add_u32 v56, v8, 1, v77
	v_mov_b32_e32 v8, v11
	ds_read_b128 v[44:47], v56
	ds_read_b128 v[48:51], v56 offset:5120
	v_mad_u64_u32 v[24:25], s[6:7], s1, v24, v[8:9]
	v_mov_b32_e32 v11, v24
	v_lshlrev_b64 v[10:11], 1, v[10:11]
	v_lshl_add_u64 v[24:25], v[2:3], 0, v[10:11]
	s_waitcnt lgkmcnt(1)
	global_store_dwordx4 v[24:25], v[44:47], off sc1
	v_lshl_add_u64 v[10:11], v[0:1], 0, v[10:11]
	v_or_b32_e32 v24, 32, v4
	s_waitcnt lgkmcnt(0)
	global_store_dwordx4 v[10:11], v[48:51], off sc1
	v_mad_u64_u32 v[10:11], s[6:7], s0, v24, 0
	ds_read_b128 v[52:55], v56 offset:1280
	ds_read_b128 v[44:47], v56 offset:2560
	v_mov_b32_e32 v8, v11
	ds_read_b128 v[48:51], v56 offset:6400
	v_mad_u64_u32 v[24:25], s[6:7], s1, v24, v[8:9]
	v_mov_b32_e32 v11, v24
	v_lshlrev_b64 v[10:11], 1, v[10:11]
	v_lshl_add_u64 v[24:25], v[2:3], 0, v[10:11]
	s_waitcnt lgkmcnt(2)
	global_store_dwordx4 v[24:25], v[52:55], off sc1
	v_lshl_add_u64 v[10:11], v[0:1], 0, v[10:11]
	v_or_b32_e32 v24, 48, v4
	ds_read_b128 v[52:55], v56 offset:7680
	s_waitcnt lgkmcnt(1)
	global_store_dwordx4 v[10:11], v[48:51], off sc1
	v_mad_u64_u32 v[10:11], s[6:7], s0, v24, 0
	v_mov_b32_e32 v8, v11
	v_mad_u64_u32 v[24:25], s[6:7], s1, v24, v[8:9]
	v_accvgpr_read_b32 v43, a32
	v_mov_b32_e32 v11, v24
	v_lshlrev_b64 v[10:11], 1, v[10:11]
	v_fma_f32 v8, s5, v43, v9
	v_lshl_add_u64 v[24:25], v[2:3], 0, v[10:11]
	v_lshl_add_u64 v[10:11], v[0:1], 0, v[10:11]
	v_max_f32_e32 v8, 0, v8
	s_waitcnt lgkmcnt(0)
	global_store_dwordx4 v[10:11], v[52:55], off sc1
	v_fma_mixlo_f16 v10, v8, s2, 0
	v_accvgpr_read_b32 v42, a33
	v_fma_mixlo_f16 v8, v8, s2, -v10 op_sel_hi:[0,0,1]
	global_store_dwordx4 v[24:25], v[44:47], off sc1
	ds_write_b16 v26, v10
	ds_write_b16 v26, v8 offset:5120
	v_fma_f32 v8, s5, v42, v9
	v_max_f32_e32 v8, 0, v8
	v_fma_mixlo_f16 v10, v8, s2, 0
	v_accvgpr_read_b32 v41, a34
	v_fma_mixlo_f16 v8, v8, s2, -v10 op_sel_hi:[0,0,1]
	ds_write_b16 v26, v10 offset:80
	ds_write_b16 v26, v8 offset:5200
	v_fma_f32 v8, s5, v41, v9
	v_max_f32_e32 v8, 0, v8
	v_fma_mixlo_f16 v10, v8, s2, 0
	v_accvgpr_read_b32 v40, a35
	v_fma_mixlo_f16 v8, v8, s2, -v10 op_sel_hi:[0,0,1]
	ds_write_b16 v26, v10 offset:160
	ds_write_b16 v26, v8 offset:5280
	v_fma_f32 v8, s5, v40, v9
	v_max_f32_e32 v8, 0, v8
	v_fma_mixlo_f16 v10, v8, s2, 0
	v_accvgpr_read_b32 v39, a36
	v_fma_mixlo_f16 v8, v8, s2, -v10 op_sel_hi:[0,0,1]
	ds_write_b16 v26, v10 offset:240
	ds_write_b16 v26, v8 offset:5360
	v_fma_f32 v8, s5, v39, v9
	v_max_f32_e32 v8, 0, v8
	v_fma_mixlo_f16 v10, v8, s2, 0
	v_accvgpr_read_b32 v38, a37
	v_fma_mixlo_f16 v8, v8, s2, -v10 op_sel_hi:[0,0,1]
	ds_write_b16 v26, v10 offset:640
	ds_write_b16 v26, v8 offset:5760
	v_fma_f32 v8, s5, v38, v9
	v_max_f32_e32 v8, 0, v8
	v_fma_mixlo_f16 v10, v8, s2, 0
	v_accvgpr_read_b32 v37, a38
	v_fma_mixlo_f16 v8, v8, s2, -v10 op_sel_hi:[0,0,1]
	ds_write_b16 v26, v10 offset:720
	ds_write_b16 v26, v8 offset:5840
	v_fma_f32 v8, s5, v37, v9
	v_max_f32_e32 v8, 0, v8
	v_fma_mixlo_f16 v10, v8, s2, 0
	v_accvgpr_read_b32 v36, a39
	v_fma_mixlo_f16 v8, v8, s2, -v10 op_sel_hi:[0,0,1]
	ds_write_b16 v26, v10 offset:800
	ds_write_b16 v26, v8 offset:5920
	v_fma_f32 v8, s5, v36, v9
	v_max_f32_e32 v8, 0, v8
	v_fma_mixlo_f16 v10, v8, s2, 0
	v_accvgpr_read_b32 v35, a40
	v_fma_mixlo_f16 v8, v8, s2, -v10 op_sel_hi:[0,0,1]
	ds_write_b16 v26, v10 offset:880
	ds_write_b16 v26, v8 offset:6000
	v_fma_f32 v8, s5, v35, v9
	v_max_f32_e32 v8, 0, v8
	v_fma_mixlo_f16 v10, v8, s2, 0
	v_accvgpr_read_b32 v34, a41
	v_fma_mixlo_f16 v8, v8, s2, -v10 op_sel_hi:[0,0,1]
	ds_write_b16 v26, v10 offset:1280
	ds_write_b16 v26, v8 offset:6400
	v_fma_f32 v8, s5, v34, v9
	v_max_f32_e32 v8, 0, v8
	v_fma_mixlo_f16 v10, v8, s2, 0
	v_accvgpr_read_b32 v33, a42
	v_fma_mixlo_f16 v8, v8, s2, -v10 op_sel_hi:[0,0,1]
	ds_write_b16 v26, v10 offset:1360
	ds_write_b16 v26, v8 offset:6480
	v_fma_f32 v8, s5, v33, v9
	v_max_f32_e32 v8, 0, v8
	v_fma_mixlo_f16 v10, v8, s2, 0
	v_accvgpr_read_b32 v32, a43
	v_fma_mixlo_f16 v8, v8, s2, -v10 op_sel_hi:[0,0,1]
	ds_write_b16 v26, v10 offset:1440
	ds_write_b16 v26, v8 offset:6560
	v_fma_f32 v8, s5, v32, v9
	v_max_f32_e32 v8, 0, v8
	v_fma_mixlo_f16 v10, v8, s2, 0
	v_accvgpr_read_b32 v31, a44
	v_fma_mixlo_f16 v8, v8, s2, -v10 op_sel_hi:[0,0,1]
	ds_write_b16 v26, v10 offset:1520
	ds_write_b16 v26, v8 offset:6640
	v_fma_f32 v8, s5, v31, v9
	v_max_f32_e32 v8, 0, v8
	v_fma_mixlo_f16 v10, v8, s2, 0
	v_accvgpr_read_b32 v30, a45
	v_fma_mixlo_f16 v8, v8, s2, -v10 op_sel_hi:[0,0,1]
	ds_write_b16 v26, v10 offset:1920
	ds_write_b16 v26, v8 offset:7040
	v_fma_f32 v8, s5, v30, v9
	v_max_f32_e32 v8, 0, v8
	v_fma_mixlo_f16 v10, v8, s2, 0
	v_accvgpr_read_b32 v29, a46
	v_fma_mixlo_f16 v8, v8, s2, -v10 op_sel_hi:[0,0,1]
	ds_write_b16 v26, v10 offset:2000
	ds_write_b16 v26, v8 offset:7120
	v_fma_f32 v8, s5, v29, v9
	v_max_f32_e32 v8, 0, v8
	v_fma_mixlo_f16 v10, v8, s2, 0
	v_accvgpr_read_b32 v28, a47
	v_fma_mixlo_f16 v8, v8, s2, -v10 op_sel_hi:[0,0,1]
	ds_write_b16 v26, v10 offset:2080
	ds_write_b16 v26, v8 offset:7200
	v_fma_f32 v8, s5, v28, v9
	v_max_f32_e32 v8, 0, v8
	v_fma_mixlo_f16 v10, v8, s2, 0
	v_accvgpr_read_b32 v27, a48
	v_fma_mixlo_f16 v8, v8, s2, -v10 op_sel_hi:[0,0,1]
	ds_write_b16 v26, v10 offset:2160
	ds_write_b16 v26, v8 offset:7280
	v_fma_f32 v8, s5, v27, v9
	v_max_f32_e32 v8, 0, v8
	v_fma_mixlo_f16 v10, v8, s2, 0
	v_accvgpr_read_b32 v23, a49
	v_fma_mixlo_f16 v8, v8, s2, -v10 op_sel_hi:[0,0,1]
	ds_write_b16 v26, v10 offset:2560
	ds_write_b16 v26, v8 offset:7680
	v_fma_f32 v8, s5, v23, v9
	v_max_f32_e32 v8, 0, v8
	v_fma_mixlo_f16 v10, v8, s2, 0
	v_accvgpr_read_b32 v22, a50
	v_fma_mixlo_f16 v8, v8, s2, -v10 op_sel_hi:[0,0,1]
	ds_write_b16 v26, v10 offset:2640
	ds_write_b16 v26, v8 offset:7760
	v_fma_f32 v8, s5, v22, v9
	v_max_f32_e32 v8, 0, v8
	v_fma_mixlo_f16 v10, v8, s2, 0
	v_accvgpr_read_b32 v21, a51
	v_fma_mixlo_f16 v8, v8, s2, -v10 op_sel_hi:[0,0,1]
	ds_write_b16 v26, v10 offset:2720
	ds_write_b16 v26, v8 offset:7840
	v_fma_f32 v8, s5, v21, v9
	v_max_f32_e32 v8, 0, v8
	v_fma_mixlo_f16 v10, v8, s2, 0
	v_accvgpr_read_b32 v20, a52
	v_fma_mixlo_f16 v8, v8, s2, -v10 op_sel_hi:[0,0,1]
	ds_write_b16 v26, v10 offset:2800
	ds_write_b16 v26, v8 offset:7920
	v_fma_f32 v8, s5, v20, v9
	v_max_f32_e32 v8, 0, v8
	v_fma_mixlo_f16 v10, v8, s2, 0
	v_accvgpr_read_b32 v19, a53
	v_fma_mixlo_f16 v8, v8, s2, -v10 op_sel_hi:[0,0,1]
	ds_write_b16 v26, v10 offset:3200
	ds_write_b16 v26, v8 offset:8320
	v_fma_f32 v8, s5, v19, v9
	v_max_f32_e32 v8, 0, v8
	v_fma_mixlo_f16 v10, v8, s2, 0
	v_accvgpr_read_b32 v18, a54
	v_fma_mixlo_f16 v8, v8, s2, -v10 op_sel_hi:[0,0,1]
	ds_write_b16 v26, v10 offset:3280
	ds_write_b16 v26, v8 offset:8400
	v_fma_f32 v8, s5, v18, v9
	v_max_f32_e32 v8, 0, v8
	v_fma_mixlo_f16 v10, v8, s2, 0
	v_accvgpr_read_b32 v17, a55
	v_fma_mixlo_f16 v8, v8, s2, -v10 op_sel_hi:[0,0,1]
	ds_write_b16 v26, v10 offset:3360
	ds_write_b16 v26, v8 offset:8480
	v_fma_f32 v8, s5, v17, v9
	v_max_f32_e32 v8, 0, v8
	v_fma_mixlo_f16 v10, v8, s2, 0
	v_accvgpr_read_b32 v16, a56
	v_fma_mixlo_f16 v8, v8, s2, -v10 op_sel_hi:[0,0,1]
	ds_write_b16 v26, v10 offset:3440
	ds_write_b16 v26, v8 offset:8560
	v_fma_f32 v8, s5, v16, v9
	v_max_f32_e32 v8, 0, v8
	v_fma_mixlo_f16 v10, v8, s2, 0
	v_accvgpr_read_b32 v15, a57
	v_fma_mixlo_f16 v8, v8, s2, -v10 op_sel_hi:[0,0,1]
	ds_write_b16 v26, v10 offset:3840
	ds_write_b16 v26, v8 offset:8960
	v_fma_f32 v8, s5, v15, v9
	v_max_f32_e32 v8, 0, v8
	v_fma_mixlo_f16 v10, v8, s2, 0
	v_accvgpr_read_b32 v14, a58
	v_fma_mixlo_f16 v8, v8, s2, -v10 op_sel_hi:[0,0,1]
	ds_write_b16 v26, v10 offset:3920
	ds_write_b16 v26, v8 offset:9040
	v_fma_f32 v8, s5, v14, v9
	v_max_f32_e32 v8, 0, v8
	v_fma_mixlo_f16 v10, v8, s2, 0
	v_accvgpr_read_b32 v13, a59
	v_fma_mixlo_f16 v8, v8, s2, -v10 op_sel_hi:[0,0,1]
	ds_write_b16 v26, v10 offset:4000
	ds_write_b16 v26, v8 offset:9120
	v_fma_f32 v8, s5, v13, v9
	v_max_f32_e32 v8, 0, v8
	v_fma_mixlo_f16 v10, v8, s2, 0
	v_accvgpr_read_b32 v12, a60
	v_fma_mixlo_f16 v8, v8, s2, -v10 op_sel_hi:[0,0,1]
	ds_write_b16 v26, v10 offset:4080
	ds_write_b16 v26, v8 offset:9200
	v_fma_f32 v8, s5, v12, v9
	v_accvgpr_read_b32 v7, a61
	v_max_f32_e32 v8, 0, v8
	v_fma_mixlo_f16 v10, v8, s2, 0
	v_fma_f32 v7, s5, v7, v9
	v_accvgpr_read_b32 v6, a62
	v_fma_mixlo_f16 v8, v8, s2, -v10 op_sel_hi:[0,0,1]
	v_max_f32_e32 v7, 0, v7
	ds_write_b16 v26, v10 offset:4480
	ds_write_b16 v26, v8 offset:9600
	v_fma_mixlo_f16 v8, v7, s2, 0
	v_fma_f32 v6, s5, v6, v9
	v_accvgpr_read_b32 v5, a63
	v_fma_mixlo_f16 v7, v7, s2, -v8 op_sel_hi:[0,0,1]
	v_max_f32_e32 v6, 0, v6
	ds_write_b16 v26, v8 offset:4560
	ds_write_b16 v26, v7 offset:9680
	v_fma_mixlo_f16 v7, v6, s2, 0
	v_fmac_f32_e32 v9, s5, v5
	v_fma_mixlo_f16 v6, v6, s2, -v7 op_sel_hi:[0,0,1]
	v_max_f32_e32 v5, 0, v9
	ds_write_b16 v26, v7 offset:4640
	ds_write_b16 v26, v6 offset:9760
	v_fma_mixlo_f16 v6, v5, s2, 0
	v_fma_mixlo_f16 v5, v5, s2, -v6 op_sel_hi:[0,0,1]
	ds_write_b16 v26, v6 offset:4720
	ds_write_b16 v26, v5 offset:9840
	v_or_b32_e32 v5, 64, v4
	v_mad_u64_u32 v[14:15], s[2:3], s0, v5, 0
	v_mov_b32_e32 v16, v15
	ds_read_b128 v[6:9], v78
	ds_read_b128 v[10:13], v78 offset:5120
	v_mad_u64_u32 v[16:17], s[2:3], s1, v5, v[16:17]
	v_mov_b32_e32 v15, v16
	v_lshlrev_b64 v[14:15], 1, v[14:15]
	v_lshl_add_u64 v[16:17], v[2:3], 0, v[14:15]
	s_waitcnt lgkmcnt(1)
	global_store_dwordx4 v[16:17], v[6:9], off sc1
	v_or_b32_e32 v5, 0x50, v4
	s_nop 0
	v_lshl_add_u64 v[6:7], v[0:1], 0, v[14:15]
	s_waitcnt lgkmcnt(0)
	global_store_dwordx4 v[6:7], v[10:13], off sc1
	v_mad_u64_u32 v[14:15], s[2:3], s0, v5, 0
	ds_read_b128 v[6:9], v56
	ds_read_b128 v[10:13], v56 offset:5120
	v_mov_b32_e32 v16, v15
	v_mad_u64_u32 v[16:17], s[2:3], s1, v5, v[16:17]
	v_mov_b32_e32 v15, v16
	v_lshlrev_b64 v[18:19], 1, v[14:15]
	v_lshl_add_u64 v[20:21], v[2:3], 0, v[18:19]
	v_lshl_add_u64 v[18:19], v[0:1], 0, v[18:19]
	v_or_b32_e32 v5, 0x60, v4
	s_waitcnt lgkmcnt(0)
	global_store_dwordx4 v[18:19], v[10:13], off sc1
	v_mad_u64_u32 v[18:19], s[2:3], s0, v5, 0
	ds_read_b128 v[14:17], v56 offset:1280
	global_store_dwordx4 v[20:21], v[6:9], off sc1
	ds_read_b128 v[10:13], v56 offset:6400
	v_mov_b32_e32 v20, v19
	v_mad_u64_u32 v[20:21], s[2:3], s1, v5, v[20:21]
	v_mov_b32_e32 v19, v20
	v_lshlrev_b64 v[18:19], 1, v[18:19]
	v_lshl_add_u64 v[20:21], v[2:3], 0, v[18:19]
	v_lshl_add_u64 v[18:19], v[0:1], 0, v[18:19]
	ds_read_b128 v[6:9], v56 offset:2560
	s_waitcnt lgkmcnt(2)
	global_store_dwordx4 v[20:21], v[14:17], off sc1
	ds_read_b128 v[14:17], v56 offset:7680
	s_waitcnt lgkmcnt(2)
	global_store_dwordx4 v[18:19], v[10:13], off sc1
	s_nop 1
	v_or_b32_e32 v11, 0x70, v4
	v_mad_u64_u32 v[4:5], s[2:3], s0, v11, 0
	v_mov_b32_e32 v10, v5
	v_mad_u64_u32 v[10:11], s[0:1], s1, v11, v[10:11]
	v_mov_b32_e32 v5, v10
	v_lshlrev_b64 v[4:5], 1, v[4:5]
	v_lshl_add_u64 v[2:3], v[2:3], 0, v[4:5]
	v_lshl_add_u64 v[0:1], v[0:1], 0, v[4:5]
	s_waitcnt lgkmcnt(1)
	global_store_dwordx4 v[2:3], v[6:9], off sc1
	s_waitcnt lgkmcnt(0)
	global_store_dwordx4 v[0:1], v[14:17], off sc1
	s_endpgm
	s_endpgm
	s_endpgm
	s_endpgm
	s_endpgm
	s_endpgm
	s_endpgm
	s_endpgm
	s_endpgm
	s_endpgm
	s_endpgm
	s_endpgm
	s_endpgm
	s_endpgm
	s_endpgm
	s_endpgm
	s_endpgm
	s_endpgm
	s_endpgm
	s_endpgm
	s_endpgm
	s_endpgm
	s_endpgm
	s_endpgm
	s_endpgm
	s_endpgm
	s_endpgm
	s_endpgm
	s_endpgm
	s_endpgm
	s_endpgm
	s_endpgm
	s_endpgm
	s_endpgm
	s_endpgm
